# PEER gather: scalar row addresses (saddr-form loads) instead of two 64-bit VALU adds per expert
# baseline (speedup 1.0000x reference)
.LBB0_716:
	s_andn2_b64 vcc, exec, s[4:5]
	v_writelane_b32 v253, s85, 34
	s_cbranch_vccnz .LBB0_798
	s_lshr_b32 s4, s27, 6
	s_mulk_i32 s4, 0x1400
	s_mov_b32 s37, s7
	s_add_i32 s27, s4, 0
	s_lshl_b64 s[4:5], s[36:37], 24
	s_add_u32 s8, s50, s4
	v_lshlrev_b32_e32 v26, 4, v21
	s_addc_u32 s9, s51, s5
	s_add_u32 s100, s8, 0x2d100000
	s_addc_u32 s101, s9, 0
	s_add_u32 s86, s8, 0x35100000
	s_addc_u32 s87, s9, 0
	v_mov_b32_e32 v27, v3
	v_lshl_add_u64 v[28:29], s[8:9], 0, v[26:27]
	s_mov_b64 s[8:9], 0x2d100000
	s_lshl_b64 s[4:5], s[36:37], 17
	v_lshl_add_u64 v[124:125], v[28:29], 0, s[8:9]
	s_mov_b64 s[8:9], 0x35100000
	v_and_b32_e32 v182, 3, v2
	v_and_b32_e32 v23, 1, v2
	v_and_b32_e32 v2, 2, v2
	v_add_u32_e32 v176, 0, v26
	s_add_u32 s4, s50, s4
	v_lshl_add_u32 v177, v21, 2, s27
	v_lshl_add_u64 v[126:127], v[28:29], 0, s[8:9]
	v_lshlrev_b32_e32 v183, 2, v182
	v_cmp_eq_u32_e64 s[42:43], 0, v23
	v_cmp_eq_u32_e64 s[44:45], 0, v2
	v_lshlrev_b32_e32 v2, 5, v21
	v_lshl_add_u64 v[26:27], s[50:51], 0, v[26:27]
	s_mov_b64 s[8:9], 0x13400000
	v_lshrrev_b32_e32 v23, 2, v21
	v_bfe_u32 v21, v21, 2, 3
	v_mov_b32_e32 v25, v3
	s_addc_u32 s5, s51, s5
	v_lshl_add_u64 v[128:129], v[26:27], 0, s[8:9]
	v_lshlrev_b32_e32 v26, 6, v23
	v_lshl_add_u32 v231, v21, 7, s27
	v_lshl_or_b32 v21, v21, 6, v183
	v_lshl_add_u64 v[24:25], s[50:51], 0, v[24:25]
	v_mov_b32_e32 v23, v3
	s_add_u32 s4, s4, 0x3d100000
	v_add_u32_e32 v245, s27, v21
	v_lshl_add_u64 v[22:23], v[24:25], 0, v[22:23]
	s_mov_b64 s[8:9], 0x24d00000
	v_mov_b32_e32 v21, v3
	s_addc_u32 s5, s5, 0
	v_lshl_add_u64 v[132:133], v[22:23], 0, s[8:9]
	v_lshl_add_u64 v[20:21], s[50:51], 0, v[20:21]
	s_mov_b64 s[8:9], 0xb000000
	s_add_u32 s37, s50, 0x3d200000
	v_lshlrev_b32_e32 v201, 5, v182
	v_lshl_add_u64 v[130:131], s[50:51], 0, v[2:3]
	v_lshl_add_u64 v[134:135], v[20:21], 0, s[8:9]
	s_mov_b64 s[8:9], 0x3d300000
	v_add_u32_e32 v184, s27, v183
	v_add_u32_e32 v185, 0x1c200, v176
	v_add_u32_e32 v186, 0x1e200, v176
	v_add_u32_e32 v187, 0x1c600, v176
	v_add_u32_e32 v188, 0x1e600, v176
	v_add_u32_e32 v189, 0x1ca00, v176
	v_add_u32_e32 v190, 0x1ea00, v176
	v_add_u32_e32 v191, 0x1ce00, v176
	v_add_u32_e32 v192, 0x1ee00, v176
	v_add_u32_e32 v193, 0x1d200, v176
	v_add_u32_e32 v194, 0x1f200, v176
	v_add_u32_e32 v195, 0x1d600, v176
	v_add_u32_e32 v196, 0x1f600, v176
	v_add_u32_e32 v197, 0x1da00, v176
	v_add_u32_e32 v198, 0x1fa00, v176
	v_add_u32_e32 v199, 0x1de00, v176
	v_add_u32_e32 v200, 0x1fe00, v176
	s_addc_u32 s73, s51, 0
	v_or_b32_e32 v202, 2, v201
	v_or_b32_e32 v203, 4, v201
	v_or_b32_e32 v204, 6, v201
	v_or_b32_e32 v205, 8, v201
	v_or_b32_e32 v220, 10, v201
	v_or_b32_e32 v221, 12, v201
	v_or_b32_e32 v222, 14, v201
	v_or_b32_e32 v223, 16, v201
	v_or_b32_e32 v224, 18, v201
	v_or_b32_e32 v225, 20, v201
	v_or_b32_e32 v226, 22, v201
	v_or_b32_e32 v227, 24, v201
	v_or_b32_e32 v228, 26, v201
	v_or_b32_e32 v229, 28, v201
	v_or_b32_e32 v230, 30, v201
	v_cmp_eq_u32_e64 s[46:47], 0, v182
	v_cmp_ne_u32_e64 s[48:49], 0, v182
	v_lshl_add_u32 v232, v182, 1, 0
	v_or_b32_e32 v233, 4, v182
	v_or_b32_e32 v234, 8, v182
	v_or_b32_e32 v235, 12, v182
	v_or_b32_e32 v236, 16, v182
	v_or_b32_e32 v237, 20, v182
	v_or_b32_e32 v238, 24, v182
	v_or_b32_e32 v239, 28, v182
	v_or_b32_e32 v240, 32, v182
	v_or_b32_e32 v241, 36, v182
	v_or_b32_e32 v242, 40, v182
	v_or_b32_e32 v243, 44, v182
	v_or_b32_e32 v244, 48, v182
	v_lshl_add_u64 v[136:137], v[130:131], 0, s[8:9]
	s_add_i32 s72, s27, 0xd20
	v_add_u32_e32 v246, s27, v26
	s_branch .LBB0_719

.LBB0_759:
	s_or_b64 exec, exec, s[8:9]
	v_bitop3_b32 v32, v28, 63, v28 bitop3:0xc
	v_bitop3_b32 v33, v29, 63, v29 bitop3:0xc
	v_bitop3_b32 v34, v30, 63, v30 bitop3:0xc
	v_bitop3_b32 v35, v31, 63, v31 bitop3:0xc
	v_lshl_add_u32 v32, v32, 1, 0
	v_lshl_add_u32 v33, v33, 1, 0
	v_lshl_add_u32 v34, v34, 1, 0
	v_lshl_add_u32 v35, v35, 1, 0
	ds_read_u16 v32, v32 offset:40960
	ds_read_u16 v33, v33 offset:40960
	ds_read_u16 v34, v34 offset:40960
	ds_read_u16 v35, v35 offset:40960
	v_cmp_lt_i32_e32 vcc, -1, v28
	s_movk_i32 s6, 0x800
	s_waitcnt lgkmcnt(2)
	v_add_u32_sdwa v37, v231, v33 dst_sel:DWORD dst_unused:UNUSED_PAD src0_sel:DWORD src1_sel:BYTE_0
	v_add_u32_sdwa v36, v231, v32 dst_sel:DWORD dst_unused:UNUSED_PAD src0_sel:DWORD src1_sel:BYTE_0
	v_lshrrev_b32_e32 v32, 8, v32
	v_lshrrev_b32_e32 v33, 8, v33
	s_waitcnt lgkmcnt(1)
	v_add_u32_sdwa v38, v231, v34 dst_sel:DWORD dst_unused:UNUSED_PAD src0_sel:DWORD src1_sel:BYTE_0
	v_lshrrev_b32_e32 v34, 8, v34
	s_waitcnt lgkmcnt(0)
	v_add_u32_sdwa v39, v231, v35 dst_sel:DWORD dst_unused:UNUSED_PAD src0_sel:DWORD src1_sel:BYTE_0
	v_lshrrev_b32_e32 v35, 8, v35
	v_add_u32_e32 v32, v231, v32
	v_add_u32_e32 v33, v231, v33
	v_add_u32_e32 v34, v231, v34
	v_add_u32_e32 v35, v231, v35
	ds_read_b32 v36, v36
	ds_read_b32 v32, v32 offset:64
	ds_read_b32 v37, v37
	ds_read_b32 v33, v33 offset:64
	ds_read_b32 v38, v38
	ds_read_b32 v34, v34 offset:64
	ds_read_b32 v39, v39
	ds_read_b32 v35, v35 offset:64
	s_waitcnt lgkmcnt(7)
	v_lshlrev_b32_e32 v36, 7, v36
	v_and_b32_e32 v36, 0x3f80, v36
	s_waitcnt lgkmcnt(6)
	v_and_b32_e32 v32, 0x7f, v32
	v_bitop3_b32 v32, v32, s38, v36 bitop3:0x36
	v_cndmask_b32_e64 v36, v218, -1, vcc
	v_bitop3_b32 v28, v36, v28, s78 bitop3:0x78
	s_waitcnt lgkmcnt(5)
	v_lshlrev_b32_e32 v36, 7, v37
	v_and_b32_e32 v36, 0x3f80, v36
	s_waitcnt lgkmcnt(4)
	v_and_b32_e32 v33, 0x7f, v33
	v_cmp_lt_i32_e32 vcc, -1, v29
	v_bitop3_b32 v33, v33, s38, v36 bitop3:0x36
	s_waitcnt lgkmcnt(2)
	v_and_b32_e32 v34, 0x7f, v34
	v_cndmask_b32_e64 v36, v218, -1, vcc
	v_bitop3_b32 v29, v36, v29, s78 bitop3:0x78
	v_lshlrev_b32_e32 v36, 7, v38
	v_and_b32_e32 v36, 0x3f80, v36
	v_cmp_lt_i32_e32 vcc, -1, v30
	v_bitop3_b32 v34, v34, s38, v36 bitop3:0x36
	v_subrev_f32_dpp v29, v28, v29 quad_perm:[0,0,0,0] row_mask:0xf bank_mask:0xf bound_ctrl:1
	v_cndmask_b32_e64 v36, v218, -1, vcc
	v_cmp_lt_i32_e32 vcc, -1, v31
	v_bitop3_b32 v30, v36, v30, s78 bitop3:0x78
	v_mul_f32_e32 v29, 0x3fb8aa3b, v29
	v_cndmask_b32_e64 v37, v218, -1, vcc
	v_bitop3_b32 v31, v37, v31, s78 bitop3:0x78
	v_subrev_f32_dpp v30, v28, v30 quad_perm:[0,0,0,0] row_mask:0xf bank_mask:0xf bound_ctrl:1
	v_subrev_f32_dpp v37, v28, v28 quad_perm:[0,0,0,0] row_mask:0xf bank_mask:0xf bound_ctrl:1
	v_mul_f32_e32 v37, 0x3fb8aa3b, v37
	v_exp_f32_e32 v37, v37
	v_exp_f32_e32 v29, v29
	v_mul_f32_e32 v30, 0x3fb8aa3b, v30
	v_subrev_f32_dpp v28, v28, v31 quad_perm:[0,0,0,0] row_mask:0xf bank_mask:0xf bound_ctrl:1
	v_exp_f32_e32 v30, v30
	v_mul_f32_e32 v28, 0x3fb8aa3b, v28
	v_exp_f32_e32 v28, v28
	v_add_f32_e32 v31, 0, v37
	v_add_f32_e32 v31, v29, v31
	v_add_f32_e32 v31, v30, v31
	v_add_f32_e32 v31, v28, v31
	s_waitcnt lgkmcnt(1)
	v_lshlrev_b32_e32 v36, 7, v39
	v_and_b32_e32 v36, 0x3f80, v36
	v_add_f32_dpp v31, v31, v31 quad_perm:[1,0,3,2] row_mask:0xf bank_mask:0xf bound_ctrl:1
	s_waitcnt lgkmcnt(0)
	v_and_b32_e32 v35, 0x7f, v35
	v_bitop3_b32 v35, v35, s38, v36 bitop3:0x36
	v_add_f32_dpp v31, v31, v31 quad_perm:[2,3,0,1] row_mask:0xf bank_mask:0xf bound_ctrl:1
	v_div_scale_f32 v38, s[8:9], v31, v31, 1.0
	v_rcp_f32_e32 v39, v38
	s_nop 0
	v_fma_f32 v36, -v38, v39, 1.0
	v_fmac_f32_e32 v39, v36, v39
	v_div_scale_f32 v36, vcc, 1.0, v31, 1.0
	v_mul_f32_e32 v40, v36, v39
	v_fma_f32 v41, -v38, v40, v36
	v_fmac_f32_e32 v40, v41, v39
	v_fma_f32 v36, -v38, v40, v36
	v_div_fmas_f32 v36, v36, v39, v40
	v_div_fixup_f32 v31, v36, v31, 1.0
	v_mul_f32_e32 v36, v37, v31
	v_mul_f32_e32 v29, v29, v31
	v_add_u32_e32 v37, 0xc00, v245
	ds_write2_b32 v37, v36, v29 offset0:192 offset1:196
	ds_write2_b32 v37, v32, v33 offset0:64 offset1:68
	v_mul_f32_e32 v29, v30, v31
	v_mul_f32_e32 v28, v28, v31
	ds_write2_b32 v37, v29, v28 offset0:200 offset1:204
	ds_write2_b32 v37, v34, v35 offset0:72 offset1:76
	s_waitcnt lgkmcnt(0)
	ds_read2st64_b32 v[28:29], v177 offset0:13 offset1:14
	ds_read2st64_b32 v[30:31], v177 offset0:15 offset1:16
	v_mov_b32_e32 v32, 0
	s_waitcnt lgkmcnt(1)
	v_cmp_gt_u32_e64 s[50:51], s6, v28
	v_cmp_gt_u32_e32 vcc, s6, v29
	s_and_saveexec_b64 s[8:9], s[50:51]
	v_mbcnt_lo_u32_b32 v32, s50, 0
	v_mbcnt_hi_u32_b32 v32, s51, v32
	s_or_b64 exec, exec, s[8:9]
	v_ashrrev_i32_e32 v33, 11, v28
	v_ashrrev_i32_e32 v34, 11, v29
	s_bcnt1_i32_b64 s6, s[50:51]
	s_bcnt1_i32_b64 s76, vcc
	s_add_i32 s76, s76, s6
	v_cmp_eq_u32_e64 s[52:53], 1, v33
	v_cmp_eq_u32_e64 s[50:51], 1, v34
	s_and_saveexec_b64 s[8:9], s[52:53]
	v_mbcnt_lo_u32_b32 v32, s52, 0
	v_mbcnt_hi_u32_b32 v32, s53, v32
	v_add_u32_e32 v32, s76, v32
	s_or_b64 exec, exec, s[8:9]
	s_bcnt1_i32_b64 s8, s[52:53]
	s_bcnt1_i32_b64 s9, s[50:51]
	s_add_i32 s76, s76, s8
	s_add_i32 s80, s76, s9
	v_cmp_eq_u32_e64 s[54:55], 2, v33
	v_cmp_eq_u32_e64 s[52:53], 2, v34
	s_and_saveexec_b64 s[8:9], s[54:55]
	v_mbcnt_lo_u32_b32 v32, s54, 0
	v_mbcnt_hi_u32_b32 v32, s55, v32
	v_add_u32_e32 v32, s80, v32
	s_or_b64 exec, exec, s[8:9]
	s_bcnt1_i32_b64 s8, s[54:55]
	s_bcnt1_i32_b64 s9, s[52:53]
	s_add_i32 s80, s80, s8
	s_add_i32 s81, s80, s9
	v_cmp_eq_u32_e64 s[56:57], 3, v33
	v_cmp_eq_u32_e64 s[54:55], 3, v34
	s_and_saveexec_b64 s[8:9], s[56:57]
	v_mbcnt_lo_u32_b32 v32, s56, 0
	v_mbcnt_hi_u32_b32 v32, s57, v32
	v_add_u32_e32 v32, s81, v32
	s_or_b64 exec, exec, s[8:9]
	s_bcnt1_i32_b64 s8, s[56:57]
	s_bcnt1_i32_b64 s9, s[54:55]
	s_add_i32 s81, s81, s8
	s_add_i32 s82, s81, s9
	v_cmp_eq_u32_e64 s[58:59], 4, v33
	v_cmp_eq_u32_e64 s[56:57], 4, v34
	s_and_saveexec_b64 s[8:9], s[58:59]
	v_mbcnt_lo_u32_b32 v32, s58, 0
	v_mbcnt_hi_u32_b32 v32, s59, v32
	v_add_u32_e32 v32, s82, v32
	s_or_b64 exec, exec, s[8:9]
	s_bcnt1_i32_b64 s8, s[58:59]
	s_bcnt1_i32_b64 s9, s[56:57]
	s_add_i32 s82, s82, s8
	s_add_i32 s84, s82, s9
	v_cmp_eq_u32_e64 s[60:61], 5, v33
	v_cmp_eq_u32_e64 s[58:59], 5, v34
	s_and_saveexec_b64 s[8:9], s[60:61]
	v_mbcnt_lo_u32_b32 v32, s60, 0
	v_mbcnt_hi_u32_b32 v32, s61, v32
	v_add_u32_e32 v32, s84, v32
	s_or_b64 exec, exec, s[8:9]
	s_bcnt1_i32_b64 s8, s[60:61]
	s_bcnt1_i32_b64 s9, s[58:59]
	s_add_i32 s84, s84, s8
	s_add_i32 s85, s84, s9
	v_cmp_eq_u32_e64 s[62:63], 6, v33
	v_cmp_eq_u32_e64 s[60:61], 6, v34
	s_and_saveexec_b64 s[8:9], s[62:63]
	v_mbcnt_lo_u32_b32 v32, s62, 0
	v_mbcnt_hi_u32_b32 v32, s63, v32
	v_add_u32_e32 v32, s85, v32
	s_or_b64 exec, exec, s[8:9]
	s_bcnt1_i32_b64 s8, s[62:63]
	s_bcnt1_i32_b64 s9, s[60:61]
	s_add_i32 s85, s85, s8
	s_add_i32 s83, s85, s9
	v_cmp_eq_u32_e64 s[64:65], 7, v33
	v_cmp_eq_u32_e64 s[62:63], 7, v34
	s_and_saveexec_b64 s[8:9], s[64:65]
	v_mbcnt_lo_u32_b32 v32, s64, 0
	v_mbcnt_hi_u32_b32 v32, s65, v32
	v_add_u32_e32 v32, s83, v32
	s_or_b64 exec, exec, s[8:9]
	v_mbcnt_lo_u32_b32 v40, vcc_lo, 0
	v_mbcnt_lo_u32_b32 v39, s50, 0
	v_mbcnt_hi_u32_b32 v40, vcc_hi, v40
	v_mbcnt_lo_u32_b32 v38, s52, 0
	v_mbcnt_hi_u32_b32 v39, s51, v39
	v_add_u32_e32 v40, s6, v40
	v_mbcnt_lo_u32_b32 v37, s54, 0
	v_mbcnt_hi_u32_b32 v38, s53, v38
	v_add_u32_e32 v39, s76, v39
	v_cndmask_b32_e32 v40, 0, v40, vcc
	v_mbcnt_lo_u32_b32 v36, s56, 0
	v_mbcnt_hi_u32_b32 v37, s55, v37
	v_add_u32_e32 v38, s80, v38
	v_cndmask_b32_e64 v39, v40, v39, s[50:51]
	v_mbcnt_lo_u32_b32 v35, s58, 0
	v_mbcnt_hi_u32_b32 v36, s57, v36
	v_add_u32_e32 v37, s81, v37
	v_cndmask_b32_e64 v38, v39, v38, s[52:53]
	v_mbcnt_lo_u32_b32 v34, s60, 0
	v_mbcnt_hi_u32_b32 v35, s59, v35
	v_add_u32_e32 v36, s82, v36
	v_cndmask_b32_e64 v37, v38, v37, s[54:55]
	v_mbcnt_lo_u32_b32 v33, s62, 0
	s_bcnt1_i32_b64 s8, s[64:65]
	v_mbcnt_hi_u32_b32 v34, s61, v34
	v_add_u32_e32 v35, s84, v35
	v_cndmask_b32_e64 v36, v37, v36, s[56:57]
	v_mbcnt_hi_u32_b32 v33, s63, v33
	v_add_u32_e32 v34, s85, v34
	v_cndmask_b32_e64 v35, v36, v35, s[58:59]
	s_add_i32 s83, s83, s8
	v_cndmask_b32_e64 v34, v35, v34, s[60:61]
	v_add_u32_e32 v33, s83, v33
	v_cndmask_b32_e64 v33, v34, v33, s[62:63]
	v_lshl_add_u32 v32, v32, 2, s27
	s_waitcnt lgkmcnt(0)
	ds_write2st64_b32 v32, v28, v30 offset0:13 offset1:15
	v_lshl_add_u32 v28, v33, 2, s27
	v_mov_b32_e32 v34, s27
	ds_write2st64_b32 v28, v29, v31 offset0:13 offset1:15
	s_waitcnt lgkmcnt(0)
	ds_read_b128 v[28:31], v34 offset:3328
	ds_read_b128 v[32:35], v34 offset:3344
	v_mov_b32_e32 v152, 0
	s_mov_b32 s6, -12
	v_mov_b32_e32 v153, v152
	s_waitcnt lgkmcnt(1)
	v_readfirstlane_b32 s8, v28
	s_ashr_i32 s9, s8, 31
	s_lshl_b64 s[8:9], s[8:9], 10
	s_add_u32 s98, s100, s8
	s_addc_u32 s99, s101, s9
	s_add_u32 s66, s86, s8
	s_addc_u32 s67, s87, s9
	v_readfirstlane_b32 s8, v29
	s_ashr_i32 s9, s8, 31
	s_lshl_b64 s[8:9], s[8:9], 10
	global_load_dwordx4 v[88:91], v176, s[98:99]
	global_load_dwordx4 v[56:59], v176, s[66:67]
	s_add_u32 s98, s100, s8
	s_addc_u32 s99, s101, s9
	s_add_u32 s66, s86, s8
	s_addc_u32 s67, s87, s9
	v_readfirstlane_b32 s8, v30
	s_ashr_i32 s9, s8, 31
	s_lshl_b64 s[8:9], s[8:9], 10
	global_load_dwordx4 v[84:87], v176, s[98:99]
	global_load_dwordx4 v[52:55], v176, s[66:67]
	s_add_u32 s98, s100, s8
	s_addc_u32 s99, s101, s9
	s_add_u32 s66, s86, s8
	s_addc_u32 s67, s87, s9
	global_load_dwordx4 v[80:83], v176, s[98:99]
	global_load_dwordx4 v[44:47], v176, s[66:67]
	v_add_u32_e32 v28, 0xc00, v184
	ds_read2_b32 v[28:29], v28 offset0:64 offset1:68
	v_readfirstlane_b32 s8, v31
	s_ashr_i32 s9, s8, 31
	s_lshl_b64 s[8:9], s[8:9], 10
	s_add_u32 s98, s100, s8
	s_addc_u32 s99, s101, s9
	s_add_u32 s66, s86, s8
	s_addc_u32 s67, s87, s9
	global_load_dwordx4 v[76:79], v176, s[98:99]
	s_nop 0
	global_load_dwordx4 v[36:39], v176, s[66:67]
	s_waitcnt lgkmcnt(0)
	v_lshlrev_b32_e32 v30, 1, v28
	v_readfirstlane_b32 s8, v32
	v_ashrrev_i32_e32 v31, 31, v30
	s_ashr_i32 s9, s8, 31
	v_lshl_add_u64 v[30:31], v[30:31], 2, s[4:5]
	s_lshl_b64 s[8:9], s[8:9], 10
	s_add_u32 s98, s100, s8
	s_addc_u32 s99, s101, s9
	global_load_dwordx2 v[140:141], v[30:31], off
	global_load_dwordx4 v[72:75], v176, s[98:99]
	s_add_u32 s66, s86, s8
	s_addc_u32 s67, s87, s9
	v_readfirstlane_b32 s8, v33
	s_ashr_i32 s9, s8, 31
	s_lshl_b64 s[8:9], s[8:9], 10
	s_add_u32 s98, s100, s8
	s_addc_u32 s99, s101, s9
	global_load_dwordx4 v[48:51], v176, s[66:67]
	global_load_dwordx4 v[68:71], v176, s[98:99]
	s_add_u32 s66, s86, s8
	s_addc_u32 s67, s87, s9
	v_readfirstlane_b32 s8, v34
	s_ashr_i32 s9, s8, 31
	s_lshl_b64 s[8:9], s[8:9], 10
	s_add_u32 s98, s100, s8
	s_addc_u32 s99, s101, s9
	global_load_dwordx4 v[40:43], v176, s[66:67]
	global_load_dwordx4 v[64:67], v176, s[98:99]
	s_add_u32 s66, s86, s8
	s_addc_u32 s67, s87, s9
	v_readfirstlane_b32 s8, v35
	s_ashr_i32 s9, s8, 31
	s_lshl_b64 s[8:9], s[8:9], 10
	s_add_u32 s98, s100, s8
	s_addc_u32 s99, s101, s9
	v_lshlrev_b32_e32 v28, 1, v29
	global_load_dwordx4 v[32:35], v176, s[66:67]
	s_nop 0
	global_load_dwordx4 v[60:63], v176, s[98:99]
	s_add_u32 s66, s86, s8
	s_addc_u32 s67, s87, s9
	v_ashrrev_i32_e32 v29, 31, v28
	v_lshl_add_u64 v[92:93], v[28:29], 2, s[4:5]
	global_load_dwordx4 v[28:31], v176, s[66:67]
	s_nop 0
	global_load_dwordx2 v[138:139], v[92:93], off
	s_mov_b32 s8, s72
	v_mov_b32_e32 v174, v152
	v_mov_b32_e32 v175, v152
	v_mov_b32_e32 v172, v152
	v_mov_b32_e32 v173, v152
	v_mov_b32_e32 v170, v152
	v_mov_b32_e32 v171, v152
	v_mov_b32_e32 v168, v152
	v_mov_b32_e32 v169, v152
	v_mov_b32_e32 v166, v152
	v_mov_b32_e32 v167, v152
	v_mov_b32_e32 v164, v152
	v_mov_b32_e32 v165, v152
	v_mov_b32_e32 v162, v152
	v_mov_b32_e32 v163, v152
	v_mov_b32_e32 v160, v152
	v_mov_b32_e32 v161, v152
	v_mov_b32_e32 v158, v152
	v_mov_b32_e32 v159, v152
	v_mov_b32_e32 v156, v152
	v_mov_b32_e32 v157, v152
	v_mov_b32_e32 v154, v152
	v_mov_b32_e32 v155, v152
	v_mov_b32_e32 v150, v152
	v_mov_b32_e32 v151, v152
	v_mov_b32_e32 v148, v152
	v_mov_b32_e32 v149, v152
	v_mov_b32_e32 v146, v152
	v_mov_b32_e32 v147, v152
	v_mov_b32_e32 v144, v152
	v_mov_b32_e32 v145, v152
.LBB0_776:
	v_mov_b32_e32 v250, s8
	ds_read_b128 v[92:95], v250
	v_add_u32_e32 v249, s8, v183
	ds_read_b32 v142, v249
	v_mov_b32_e32 v251, 0
	v_mov_b32_e32 v252, 0
	s_waitcnt lgkmcnt(1)
	v_readfirstlane_b32 s50, v92
	s_ashr_i32 s51, s50, 31
	s_lshl_b64 s[50:51], s[50:51], 10
	s_add_u32 s98, s100, s50
	s_addc_u32 s99, s101, s51
	s_add_u32 s66, s86, s50
	s_addc_u32 s67, s87, s51
	v_readfirstlane_b32 s50, v93
	s_ashr_i32 s51, s50, 31
	s_lshl_b64 s[50:51], s[50:51], 10
	global_load_dwordx4 v[120:123], v176, s[98:99]
	global_load_dwordx4 v[104:107], v176, s[66:67]
	s_add_u32 s98, s100, s50
	s_addc_u32 s99, s101, s51
	s_add_u32 s66, s86, s50
	s_addc_u32 s67, s87, s51
	v_readfirstlane_b32 s50, v94
	s_ashr_i32 s51, s50, 31
	s_lshl_b64 s[50:51], s[50:51], 10
	global_load_dwordx4 v[116:119], v176, s[98:99]
	global_load_dwordx4 v[100:103], v176, s[66:67]
	s_add_u32 s98, s100, s50
	s_addc_u32 s99, s101, s51
	s_add_u32 s66, s86, s50
	s_addc_u32 s67, s87, s51
	v_readfirstlane_b32 s50, v95
	s_ashr_i32 s51, s50, 31
	s_lshl_b64 s[50:51], s[50:51], 10
	s_waitcnt lgkmcnt(0)
	v_lshlrev_b32_e32 v142, 1, v142
	global_load_dwordx4 v[112:115], v176, s[98:99]
	s_nop 0
	global_load_dwordx4 v[96:99], v176, s[66:67]
	s_add_u32 s98, s100, s50
	s_addc_u32 s99, s101, s51
	s_add_u32 s66, s86, s50
	s_addc_u32 s67, s87, s51
	v_ashrrev_i32_e32 v143, 31, v142
	global_load_dwordx4 v[108:111], v176, s[98:99]
	s_nop 0
	global_load_dwordx4 v[92:95], v176, s[66:67]
	v_lshl_add_u64 v[142:143], v[142:143], 2, s[4:5]
	global_load_dwordx2 v[142:143], v[142:143], off
	s_waitcnt vmcnt(26)
	v_dot8c_i32_i4_e32 v251, v88, v24
	v_dot8c_i32_i4_e32 v252, v88, v20
	v_dot8c_i32_i4_e32 v251, v89, v25
	v_dot8c_i32_i4_e32 v252, v89, v21
	v_dot8c_i32_i4_e32 v251, v90, v26
	v_dot8c_i32_i4_e32 v252, v90, v22
	v_mov_b32_e32 v89, 0
	v_mov_b32_e32 v90, 0
	s_waitcnt vmcnt(24)
	v_dot8c_i32_i4_e32 v89, v84, v24
	v_dot8c_i32_i4_e32 v90, v84, v20
	v_dot8c_i32_i4_e32 v89, v85, v25
	v_dot8c_i32_i4_e32 v90, v85, v21
	v_dot8c_i32_i4_e32 v89, v86, v26
	v_dot8c_i32_i4_e32 v90, v86, v22
	v_mov_b32_e32 v85, 0
	v_mov_b32_e32 v86, 0
	s_waitcnt vmcnt(21)
	v_dot8c_i32_i4_e32 v85, v80, v24
	v_dot8c_i32_i4_e32 v86, v80, v20
	v_dot8c_i32_i4_e32 v85, v81, v25
	v_dot8c_i32_i4_e32 v86, v81, v21
	v_dot8c_i32_i4_e32 v85, v82, v26
	v_dot8c_i32_i4_e32 v86, v82, v22
	v_mov_b32_e32 v81, 0
	v_mov_b32_e32 v82, 0
	s_waitcnt vmcnt(19)
	v_dot8c_i32_i4_e32 v81, v76, v24
	v_dot8c_i32_i4_e32 v82, v76, v20
	v_dot8c_i32_i4_e32 v81, v77, v25
	v_dot8c_i32_i4_e32 v82, v77, v21
	v_dot8c_i32_i4_e32 v251, v91, v27
	v_dot8c_i32_i4_e32 v252, v91, v23
	v_dot8c_i32_i4_e32 v89, v87, v27
	v_dot8c_i32_i4_e32 v90, v87, v23
	v_dot8c_i32_i4_e32 v81, v78, v26
	v_dot8c_i32_i4_e32 v82, v78, v22
	v_lshl_add_u32 v88, v251, 4, v252
	v_lshl_add_u32 v84, v89, 4, v90
	v_dot8c_i32_i4_e32 v85, v83, v27
	v_dot8c_i32_i4_e32 v86, v83, v23
	v_dot8c_i32_i4_e32 v81, v79, v27
	v_dot8c_i32_i4_e32 v82, v79, v23
	v_cvt_f32_i32_e32 v88, v88
	v_cvt_f32_i32_e32 v84, v84
	v_lshl_add_u32 v80, v85, 4, v86
	v_lshl_add_u32 v76, v81, 4, v82
	v_cvt_f32_i32_e32 v80, v80
	v_cvt_f32_i32_e32 v76, v76
	v_cndmask_b32_e64 v77, v84, v88, s[42:43]
	v_cndmask_b32_e64 v78, v88, v84, s[42:43]
	s_nop 1
	v_add_f32_dpp v77, v78, v77 quad_perm:[1,0,3,2] row_mask:0xf bank_mask:0xf bound_ctrl:1
	v_cndmask_b32_e64 v78, v76, v80, s[42:43]
	v_cndmask_b32_e64 v76, v80, v76, s[42:43]
	s_nop 1
	v_add_f32_dpp v76, v76, v78 quad_perm:[1,0,3,2] row_mask:0xf bank_mask:0xf bound_ctrl:1
	v_cndmask_b32_e64 v78, v76, v77, s[44:45]
	v_cndmask_b32_e64 v76, v77, v76, s[44:45]
	s_nop 1
	v_add_f32_dpp v76, v76, v78 quad_perm:[2,3,0,1] row_mask:0xf bank_mask:0xf bound_ctrl:1
	s_nop 1
	v_add_f32_dpp v76, v76, v76 row_ror:4 row_mask:0xf bank_mask:0xf bound_ctrl:1
	s_nop 1
	v_add_f32_dpp v76, v76, v76 row_ror:8 row_mask:0xf bank_mask:0xf bound_ctrl:1
	v_mov_b32_e32 v77, v76
	s_nop 1
	v_permlane32_swap_b32_e32 v76, v77
	v_add_f32_e32 v76, v76, v77
	v_mov_b32_e32 v77, v76
	s_nop 1
	v_permlane16_swap_b32_e32 v76, v77
	v_add_f32_e32 v76, v76, v77
	s_waitcnt vmcnt(18)
	v_mul_f32_e32 v77, v248, v140
	v_mul_f32_e32 v76, v77, v76
	v_fma_f32 v77, |v76|, s39, 1.0
	v_rcp_f32_e32 v77, v77
	v_mul_f32_e32 v80, v76, v76
	v_mul_f32_e32 v80, 0xbf38aa3b, v80
	v_exp_f32_e32 v80, v80
	v_fmamk_f32 v79, v77, 0x3f07dc22, v210
	v_fmaak_f32 v79, v77, v79, 0x3f35f0e3
	v_fmaak_f32 v79, v77, v79, 0xbe11a98e
	ds_read_b32 v78, v249 offset:480
	v_fmaak_f32 v79, v77, v79, 0x3e027906
	v_mul_f32_e32 v77, v77, v79
	v_mul_f32_e32 v77, v80, v77
	v_mul_f32_e32 v79, v76, v77
	v_fma_f32 v77, -v76, v77, v76
	v_cmp_gt_f32_e32 vcc, 0, v76
	s_nop 1
	v_cndmask_b32_e32 v76, v77, v79, vcc
	s_waitcnt lgkmcnt(0)
	v_mul_f32_e32 v76, v78, v76
	v_mul_f32_e32 v251, v141, v76
	s_nop 0
	v_readlane_b32 s50, v251, 0
	v_cvt_scalef32_pk_f32_fp4 v[76:77], v56, 1.0
	v_cvt_scalef32_pk_f32_fp4 v[78:79], v56, 1.0 op_sel:[1,0,0]
	v_cvt_scalef32_pk_f32_fp4 v[80:81], v56, 1.0 op_sel:[0,1,0]
	v_cvt_scalef32_pk_f32_fp4 v[82:83], v56, 1.0 op_sel:[1,1,0]
	v_pk_fma_f32 v[76:77], v[76:77], s[50:51], v[152:153] op_sel_hi:[1,0,1]
	v_cvt_scalef32_pk_f32_fp4 v[84:85], v57, 1.0
	v_cvt_scalef32_pk_f32_fp4 v[86:87], v57, 1.0 op_sel:[1,0,0]
	v_cvt_scalef32_pk_f32_fp4 v[88:89], v57, 1.0 op_sel:[0,1,0]
	v_cvt_scalef32_pk_f32_fp4 v[56:57], v57, 1.0 op_sel:[1,1,0]
	v_cvt_scalef32_pk_f32_fp4 v[90:91], v58, 1.0
	v_cvt_scalef32_pk_f32_fp4 v[140:141], v58, 1.0 op_sel:[1,0,0]
	v_cvt_scalef32_pk_f32_fp4 v[152:153], v58, 1.0 op_sel:[0,1,0]
	v_pk_fma_f32 v[56:57], v[56:57], s[50:51], v[162:163] op_sel_hi:[1,0,1]
	v_cvt_scalef32_pk_f32_fp4 v[162:163], v58, 1.0 op_sel:[1,1,0]
	v_pk_fma_f32 v[90:91], v[90:91], s[50:51], v[160:161] op_sel_hi:[1,0,1]
	v_pk_fma_f32 v[140:141], v[140:141], s[50:51], v[158:159] op_sel_hi:[1,0,1]
	v_pk_fma_f32 v[152:153], v[152:153], s[50:51], v[156:157] op_sel_hi:[1,0,1]
	v_cvt_scalef32_pk_f32_fp4 v[156:157], v59, 1.0
	v_cvt_scalef32_pk_f32_fp4 v[158:159], v59, 1.0 op_sel:[1,0,0]
	v_cvt_scalef32_pk_f32_fp4 v[160:161], v59, 1.0 op_sel:[0,1,0]
	v_cvt_scalef32_pk_f32_fp4 v[58:59], v59, 1.0 op_sel:[1,1,0]
	v_pk_fma_f32 v[78:79], v[78:79], s[50:51], v[174:175] op_sel_hi:[1,0,1]
	v_pk_fma_f32 v[80:81], v[80:81], s[50:51], v[172:173] op_sel_hi:[1,0,1]
	v_pk_fma_f32 v[82:83], v[82:83], s[50:51], v[170:171] op_sel_hi:[1,0,1]
	v_pk_fma_f32 v[84:85], v[84:85], s[50:51], v[168:169] op_sel_hi:[1,0,1]
	v_pk_fma_f32 v[86:87], v[86:87], s[50:51], v[166:167] op_sel_hi:[1,0,1]
	v_pk_fma_f32 v[88:89], v[88:89], s[50:51], v[164:165] op_sel_hi:[1,0,1]
	v_pk_fma_f32 v[154:155], v[162:163], s[50:51], v[154:155] op_sel_hi:[1,0,1]
	v_pk_fma_f32 v[150:151], v[156:157], s[50:51], v[150:151] op_sel_hi:[1,0,1]
	v_pk_fma_f32 v[148:149], v[158:159], s[50:51], v[148:149] op_sel_hi:[1,0,1]
	v_pk_fma_f32 v[146:147], v[160:161], s[50:51], v[146:147] op_sel_hi:[1,0,1]
	v_pk_fma_f32 v[58:59], v[58:59], s[50:51], v[144:145] op_sel_hi:[1,0,1]
	v_readlane_b32 s50, v251, 1
	v_cvt_scalef32_pk_f32_fp4 v[144:145], v52, 1.0
	v_cvt_scalef32_pk_f32_fp4 v[156:157], v52, 1.0 op_sel:[1,0,0]
	v_cvt_scalef32_pk_f32_fp4 v[158:159], v52, 1.0 op_sel:[0,1,0]
	v_cvt_scalef32_pk_f32_fp4 v[160:161], v52, 1.0 op_sel:[1,1,0]
	v_pk_fma_f32 v[76:77], v[144:145], s[50:51], v[76:77] op_sel_hi:[1,0,1]
	v_pk_fma_f32 v[78:79], v[156:157], s[50:51], v[78:79] op_sel_hi:[1,0,1]
	v_pk_fma_f32 v[80:81], v[158:159], s[50:51], v[80:81] op_sel_hi:[1,0,1]
	v_cvt_scalef32_pk_f32_fp4 v[144:145], v53, 1.0
	v_cvt_scalef32_pk_f32_fp4 v[156:157], v53, 1.0 op_sel:[1,0,0]
	v_cvt_scalef32_pk_f32_fp4 v[158:159], v53, 1.0 op_sel:[0,1,0]
	v_cvt_scalef32_pk_f32_fp4 v[52:53], v53, 1.0 op_sel:[1,1,0]
	v_pk_fma_f32 v[84:85], v[144:145], s[50:51], v[84:85] op_sel_hi:[1,0,1]
	v_pk_fma_f32 v[86:87], v[156:157], s[50:51], v[86:87] op_sel_hi:[1,0,1]
	v_pk_fma_f32 v[88:89], v[158:159], s[50:51], v[88:89] op_sel_hi:[1,0,1]
	v_pk_fma_f32 v[52:53], v[52:53], s[50:51], v[56:57] op_sel_hi:[1,0,1]
	v_cvt_scalef32_pk_f32_fp4 v[56:57], v54, 1.0
	v_cvt_scalef32_pk_f32_fp4 v[144:145], v54, 1.0 op_sel:[1,0,0]
	v_cvt_scalef32_pk_f32_fp4 v[156:157], v54, 1.0 op_sel:[0,1,0]
	v_cvt_scalef32_pk_f32_fp4 v[158:159], v54, 1.0 op_sel:[1,1,0]
	v_pk_fma_f32 v[56:57], v[56:57], s[50:51], v[90:91] op_sel_hi:[1,0,1]
	v_pk_fma_f32 v[90:91], v[144:145], s[50:51], v[140:141] op_sel_hi:[1,0,1]
	v_pk_fma_f32 v[140:141], v[156:157], s[50:51], v[152:153] op_sel_hi:[1,0,1]
	v_pk_fma_f32 v[144:145], v[158:159], s[50:51], v[154:155] op_sel_hi:[1,0,1]
	v_cvt_scalef32_pk_f32_fp4 v[152:153], v55, 1.0
	v_cvt_scalef32_pk_f32_fp4 v[154:155], v55, 1.0 op_sel:[1,0,0]
	v_cvt_scalef32_pk_f32_fp4 v[156:157], v55, 1.0 op_sel:[0,1,0]
	v_cvt_scalef32_pk_f32_fp4 v[54:55], v55, 1.0 op_sel:[1,1,0]
	v_pk_fma_f32 v[82:83], v[160:161], s[50:51], v[82:83] op_sel_hi:[1,0,1]
	v_pk_fma_f32 v[150:151], v[152:153], s[50:51], v[150:151] op_sel_hi:[1,0,1]
	v_pk_fma_f32 v[148:149], v[154:155], s[50:51], v[148:149] op_sel_hi:[1,0,1]
	v_pk_fma_f32 v[146:147], v[156:157], s[50:51], v[146:147] op_sel_hi:[1,0,1]
	v_pk_fma_f32 v[54:55], v[54:55], s[50:51], v[58:59] op_sel_hi:[1,0,1]
	v_readlane_b32 s50, v251, 2
	v_cvt_scalef32_pk_f32_fp4 v[58:59], v44, 1.0
	v_cvt_scalef32_pk_f32_fp4 v[152:153], v44, 1.0 op_sel:[1,0,0]
	v_cvt_scalef32_pk_f32_fp4 v[154:155], v44, 1.0 op_sel:[0,1,0]
	v_cvt_scalef32_pk_f32_fp4 v[156:157], v44, 1.0 op_sel:[1,1,0]
	v_pk_fma_f32 v[58:59], v[58:59], s[50:51], v[76:77] op_sel_hi:[1,0,1]
	v_pk_fma_f32 v[76:77], v[152:153], s[50:51], v[78:79] op_sel_hi:[1,0,1]
	v_pk_fma_f32 v[78:79], v[154:155], s[50:51], v[80:81] op_sel_hi:[1,0,1]
	v_pk_fma_f32 v[80:81], v[156:157], s[50:51], v[82:83] op_sel_hi:[1,0,1]
	v_cvt_scalef32_pk_f32_fp4 v[82:83], v45, 1.0
	v_cvt_scalef32_pk_f32_fp4 v[152:153], v45, 1.0 op_sel:[1,0,0]
	v_cvt_scalef32_pk_f32_fp4 v[154:155], v45, 1.0 op_sel:[0,1,0]
	v_cvt_scalef32_pk_f32_fp4 v[44:45], v45, 1.0 op_sel:[1,1,0]
	v_pk_fma_f32 v[82:83], v[82:83], s[50:51], v[84:85] op_sel_hi:[1,0,1]
	v_pk_fma_f32 v[84:85], v[152:153], s[50:51], v[86:87] op_sel_hi:[1,0,1]
	v_pk_fma_f32 v[86:87], v[154:155], s[50:51], v[88:89] op_sel_hi:[1,0,1]
	v_pk_fma_f32 v[44:45], v[44:45], s[50:51], v[52:53] op_sel_hi:[1,0,1]
	v_cvt_scalef32_pk_f32_fp4 v[52:53], v46, 1.0
	v_cvt_scalef32_pk_f32_fp4 v[88:89], v46, 1.0 op_sel:[1,0,0]
	v_cvt_scalef32_pk_f32_fp4 v[152:153], v46, 1.0 op_sel:[0,1,0]
	v_cvt_scalef32_pk_f32_fp4 v[154:155], v46, 1.0 op_sel:[1,1,0]
	v_pk_fma_f32 v[52:53], v[52:53], s[50:51], v[56:57] op_sel_hi:[1,0,1]
	v_pk_fma_f32 v[56:57], v[88:89], s[50:51], v[90:91] op_sel_hi:[1,0,1]
	v_pk_fma_f32 v[88:89], v[152:153], s[50:51], v[140:141] op_sel_hi:[1,0,1]
	v_pk_fma_f32 v[90:91], v[154:155], s[50:51], v[144:145] op_sel_hi:[1,0,1]
	v_cvt_scalef32_pk_f32_fp4 v[140:141], v47, 1.0
	v_cvt_scalef32_pk_f32_fp4 v[144:145], v47, 1.0 op_sel:[1,0,0]
	v_cvt_scalef32_pk_f32_fp4 v[152:153], v47, 1.0 op_sel:[0,1,0]
	v_cvt_scalef32_pk_f32_fp4 v[46:47], v47, 1.0 op_sel:[1,1,0]
	v_pk_fma_f32 v[140:141], v[140:141], s[50:51], v[150:151] op_sel_hi:[1,0,1]
	v_pk_fma_f32 v[170:171], v[144:145], s[50:51], v[148:149] op_sel_hi:[1,0,1]
	v_pk_fma_f32 v[172:173], v[152:153], s[50:51], v[146:147] op_sel_hi:[1,0,1]
	v_pk_fma_f32 v[46:47], v[46:47], s[50:51], v[54:55] op_sel_hi:[1,0,1]
	v_readlane_b32 s50, v251, 3
	v_cvt_scalef32_pk_f32_fp4 v[54:55], v36, 1.0
	v_cvt_scalef32_pk_f32_fp4 v[146:147], v36, 1.0 op_sel:[1,0,0]
	v_cvt_scalef32_pk_f32_fp4 v[148:149], v36, 1.0 op_sel:[0,1,0]
	v_cvt_scalef32_pk_f32_fp4 v[150:151], v36, 1.0 op_sel:[1,1,0]
	v_pk_fma_f32 v[144:145], v[54:55], s[50:51], v[58:59] op_sel_hi:[1,0,1]
	v_pk_fma_f32 v[146:147], v[146:147], s[50:51], v[76:77] op_sel_hi:[1,0,1]
	v_cvt_scalef32_pk_f32_fp4 v[54:55], v37, 1.0
	v_cvt_scalef32_pk_f32_fp4 v[58:59], v37, 1.0 op_sel:[1,0,0]
	v_cvt_scalef32_pk_f32_fp4 v[76:77], v37, 1.0 op_sel:[0,1,0]
	v_cvt_scalef32_pk_f32_fp4 v[36:37], v37, 1.0 op_sel:[1,1,0]
	v_pk_fma_f32 v[158:159], v[36:37], s[50:51], v[44:45] op_sel_hi:[1,0,1]
	v_cvt_scalef32_pk_f32_fp4 v[36:37], v38, 1.0
	v_cvt_scalef32_pk_f32_fp4 v[44:45], v38, 1.0 op_sel:[1,0,0]
	v_pk_fma_f32 v[152:153], v[54:55], s[50:51], v[82:83] op_sel_hi:[1,0,1]
	v_pk_fma_f32 v[154:155], v[58:59], s[50:51], v[84:85] op_sel_hi:[1,0,1]
	v_cvt_scalef32_pk_f32_fp4 v[54:55], v38, 1.0 op_sel:[0,1,0]
	v_cvt_scalef32_pk_f32_fp4 v[58:59], v38, 1.0 op_sel:[1,1,0]
	v_pk_fma_f32 v[160:161], v[36:37], s[50:51], v[52:53] op_sel_hi:[1,0,1]
	v_pk_fma_f32 v[162:163], v[44:45], s[50:51], v[56:57] op_sel_hi:[1,0,1]
	v_cvt_scalef32_pk_f32_fp4 v[36:37], v39, 1.0
	v_cvt_scalef32_pk_f32_fp4 v[44:45], v39, 1.0 op_sel:[1,0,0]
	v_cvt_scalef32_pk_f32_fp4 v[52:53], v39, 1.0 op_sel:[0,1,0]
	v_cvt_scalef32_pk_f32_fp4 v[38:39], v39, 1.0 op_sel:[1,1,0]
	v_pk_fma_f32 v[148:149], v[148:149], s[50:51], v[78:79] op_sel_hi:[1,0,1]
	v_pk_fma_f32 v[150:151], v[150:151], s[50:51], v[80:81] op_sel_hi:[1,0,1]
	v_pk_fma_f32 v[156:157], v[76:77], s[50:51], v[86:87] op_sel_hi:[1,0,1]
	v_pk_fma_f32 v[164:165], v[54:55], s[50:51], v[88:89] op_sel_hi:[1,0,1]
	v_pk_fma_f32 v[166:167], v[58:59], s[50:51], v[90:91] op_sel_hi:[1,0,1]
	v_pk_fma_f32 v[168:169], v[36:37], s[50:51], v[140:141] op_sel_hi:[1,0,1]
	v_pk_fma_f32 v[170:171], v[44:45], s[50:51], v[170:171] op_sel_hi:[1,0,1]
	v_pk_fma_f32 v[172:173], v[52:53], s[50:51], v[172:173] op_sel_hi:[1,0,1]
	v_pk_fma_f32 v[174:175], v[38:39], s[50:51], v[46:47] op_sel_hi:[1,0,1]
	ds_read_b128 v[36:39], v250 offset:16
	ds_read_b32 v140, v249 offset:16
	v_mov_b32_e32 v251, 0
	v_mov_b32_e32 v252, 0
	s_waitcnt vmcnt(17)
	v_dot8c_i32_i4_e32 v251, v72, v24
	s_waitcnt lgkmcnt(1)
	v_readfirstlane_b32 s50, v36
	s_ashr_i32 s51, s50, 31
	s_lshl_b64 s[50:51], s[50:51], 10
	s_add_u32 s98, s100, s50
	s_addc_u32 s99, s101, s51
	global_load_dwordx4 v[88:91], v176, s[98:99]
	s_add_u32 s66, s86, s50
	s_addc_u32 s67, s87, s51
	v_readfirstlane_b32 s50, v37
	s_ashr_i32 s51, s50, 31
	s_lshl_b64 s[50:51], s[50:51], 10
	s_add_u32 s98, s100, s50
	s_addc_u32 s99, s101, s51
	global_load_dwordx4 v[56:59], v176, s[66:67]
	global_load_dwordx4 v[84:87], v176, s[98:99]
	s_add_u32 s66, s86, s50
	s_addc_u32 s67, s87, s51
	v_readfirstlane_b32 s50, v38
	s_waitcnt lgkmcnt(0)
	v_lshlrev_b32_e32 v140, 1, v140
	s_ashr_i32 s51, s50, 31
	v_ashrrev_i32_e32 v141, 31, v140
	s_lshl_b64 s[50:51], s[50:51], 10
	v_lshl_add_u64 v[140:141], v[140:141], 2, s[4:5]
	global_load_dwordx4 v[52:55], v176, s[66:67]
	v_dot8c_i32_i4_e32 v252, v72, v20
	global_load_dwordx2 v[140:141], v[140:141], off
	s_add_u32 s98, s100, s50
	s_addc_u32 s99, s101, s51
	global_load_dwordx4 v[80:83], v176, s[98:99]
	s_add_u32 s66, s86, s50
	s_addc_u32 s67, s87, s51
	v_readfirstlane_b32 s50, v39
	s_ashr_i32 s51, s50, 31
	s_lshl_b64 s[50:51], s[50:51], 10
	global_load_dwordx4 v[44:47], v176, s[66:67]
	s_add_u32 s98, s100, s50
	s_addc_u32 s99, s101, s51
	global_load_dwordx4 v[76:79], v176, s[98:99]
	s_add_u32 s66, s86, s50
	s_addc_u32 s67, s87, s51
	global_load_dwordx4 v[36:39], v176, s[66:67]
	v_dot8c_i32_i4_e32 v251, v73, v25
	v_dot8c_i32_i4_e32 v252, v73, v21
	v_dot8c_i32_i4_e32 v251, v74, v26
	v_dot8c_i32_i4_e32 v252, v74, v22
	v_mov_b32_e32 v73, 0
	v_mov_b32_e32 v74, 0
	s_waitcnt vmcnt(24)
	v_dot8c_i32_i4_e32 v73, v68, v24
	v_dot8c_i32_i4_e32 v74, v68, v20
	v_dot8c_i32_i4_e32 v73, v69, v25
	v_dot8c_i32_i4_e32 v74, v69, v21
	v_dot8c_i32_i4_e32 v73, v70, v26
	v_dot8c_i32_i4_e32 v74, v70, v22
	v_mov_b32_e32 v69, 0
	v_mov_b32_e32 v70, 0
	s_waitcnt vmcnt(21)
	v_dot8c_i32_i4_e32 v69, v64, v24
	v_dot8c_i32_i4_e32 v70, v64, v20
	v_dot8c_i32_i4_e32 v69, v65, v25
	v_dot8c_i32_i4_e32 v70, v65, v21
	v_dot8c_i32_i4_e32 v69, v66, v26
	v_dot8c_i32_i4_e32 v70, v66, v22
	v_mov_b32_e32 v65, 0
	v_mov_b32_e32 v66, 0
	s_waitcnt vmcnt(19)
	v_dot8c_i32_i4_e32 v65, v60, v24
	v_dot8c_i32_i4_e32 v66, v60, v20
	v_dot8c_i32_i4_e32 v65, v61, v25
	v_dot8c_i32_i4_e32 v66, v61, v21
	v_dot8c_i32_i4_e32 v251, v75, v27
	v_dot8c_i32_i4_e32 v252, v75, v23
	v_dot8c_i32_i4_e32 v73, v71, v27
	v_dot8c_i32_i4_e32 v74, v71, v23
	v_dot8c_i32_i4_e32 v65, v62, v26
	v_dot8c_i32_i4_e32 v66, v62, v22
	v_lshl_add_u32 v72, v251, 4, v252
	v_lshl_add_u32 v68, v73, 4, v74
	v_dot8c_i32_i4_e32 v69, v67, v27
	v_dot8c_i32_i4_e32 v70, v67, v23
	v_dot8c_i32_i4_e32 v65, v63, v27
	v_dot8c_i32_i4_e32 v66, v63, v23
	v_cvt_f32_i32_e32 v72, v72
	v_cvt_f32_i32_e32 v68, v68
	v_lshl_add_u32 v64, v69, 4, v70
	v_lshl_add_u32 v60, v65, 4, v66
	v_cvt_f32_i32_e32 v64, v64
	v_cvt_f32_i32_e32 v60, v60
	v_cndmask_b32_e64 v61, v68, v72, s[42:43]
	v_cndmask_b32_e64 v62, v72, v68, s[42:43]
	s_nop 1
	v_add_f32_dpp v61, v62, v61 quad_perm:[1,0,3,2] row_mask:0xf bank_mask:0xf bound_ctrl:1
	v_cndmask_b32_e64 v62, v60, v64, s[42:43]
	v_cndmask_b32_e64 v60, v64, v60, s[42:43]
	s_nop 1
	v_add_f32_dpp v60, v60, v62 quad_perm:[1,0,3,2] row_mask:0xf bank_mask:0xf bound_ctrl:1
	v_cndmask_b32_e64 v62, v60, v61, s[44:45]
	v_cndmask_b32_e64 v60, v61, v60, s[44:45]
	s_nop 1
	v_add_f32_dpp v60, v60, v62 quad_perm:[2,3,0,1] row_mask:0xf bank_mask:0xf bound_ctrl:1
	s_waitcnt vmcnt(18)
	v_mul_f32_e32 v62, v248, v138
	v_add_f32_dpp v60, v60, v60 row_ror:4 row_mask:0xf bank_mask:0xf bound_ctrl:1
	s_nop 1
	v_add_f32_dpp v60, v60, v60 row_ror:8 row_mask:0xf bank_mask:0xf bound_ctrl:1
	v_mov_b32_e32 v61, v60
	s_nop 1
	v_permlane32_swap_b32_e32 v60, v61
	v_add_f32_e32 v60, v60, v61
	v_mov_b32_e32 v61, v60
	s_nop 1
	v_permlane16_swap_b32_e32 v60, v61
	v_add_f32_e32 v60, v60, v61
	ds_read_b32 v61, v249 offset:496
	v_mul_f32_e32 v60, v62, v60
	v_fma_f32 v62, |v60|, s39, 1.0
	v_rcp_f32_e32 v62, v62
	v_cmp_gt_f32_e32 vcc, 0, v60
	v_fmamk_f32 v63, v62, 0x3f07dc22, v210
	v_fmaak_f32 v63, v62, v63, 0x3f35f0e3
	v_fmaak_f32 v63, v62, v63, 0xbe11a98e
	v_fmaak_f32 v63, v62, v63, 0x3e027906
	v_mul_f32_e32 v62, v62, v63
	v_mul_f32_e32 v63, v60, v60
	v_mul_f32_e32 v63, 0xbf38aa3b, v63
	v_exp_f32_e32 v63, v63
	s_nop 0
	v_mul_f32_e32 v62, v63, v62
	v_mul_f32_e32 v63, v60, v62
	v_fma_f32 v60, -v60, v62, v60
	v_cndmask_b32_e32 v60, v60, v63, vcc
	s_waitcnt lgkmcnt(0)
	v_mul_f32_e32 v60, v61, v60
	v_mul_f32_e32 v251, v139, v60
	s_nop 0
	v_readlane_b32 s50, v251, 0
	v_cvt_scalef32_pk_f32_fp4 v[60:61], v48, 1.0
	v_cvt_scalef32_pk_f32_fp4 v[62:63], v48, 1.0 op_sel:[1,0,0]
	v_cvt_scalef32_pk_f32_fp4 v[64:65], v48, 1.0 op_sel:[0,1,0]
	v_cvt_scalef32_pk_f32_fp4 v[66:67], v48, 1.0 op_sel:[1,1,0]
	v_cvt_scalef32_pk_f32_fp4 v[68:69], v49, 1.0
	v_pk_fma_f32 v[60:61], v[60:61], s[50:51], v[144:145] op_sel_hi:[1,0,1]
	v_pk_fma_f32 v[62:63], v[62:63], s[50:51], v[146:147] op_sel_hi:[1,0,1]
	v_pk_fma_f32 v[64:65], v[64:65], s[50:51], v[148:149] op_sel_hi:[1,0,1]
	v_pk_fma_f32 v[66:67], v[66:67], s[50:51], v[150:151] op_sel_hi:[1,0,1]
	v_cvt_scalef32_pk_f32_fp4 v[70:71], v49, 1.0 op_sel:[1,0,0]
	v_cvt_scalef32_pk_f32_fp4 v[72:73], v49, 1.0 op_sel:[0,1,0]
	v_cvt_scalef32_pk_f32_fp4 v[48:49], v49, 1.0 op_sel:[1,1,0]
	v_pk_fma_f32 v[68:69], v[68:69], s[50:51], v[152:153] op_sel_hi:[1,0,1]
	v_cvt_scalef32_pk_f32_fp4 v[74:75], v50, 1.0
	v_cvt_scalef32_pk_f32_fp4 v[138:139], v50, 1.0 op_sel:[1,0,0]
	v_cvt_scalef32_pk_f32_fp4 v[144:145], v50, 1.0 op_sel:[0,1,0]
	v_cvt_scalef32_pk_f32_fp4 v[146:147], v50, 1.0 op_sel:[1,1,0]
	v_cvt_scalef32_pk_f32_fp4 v[148:149], v51, 1.0
	v_cvt_scalef32_pk_f32_fp4 v[150:151], v51, 1.0 op_sel:[1,0,0]
	v_cvt_scalef32_pk_f32_fp4 v[152:153], v51, 1.0 op_sel:[0,1,0]
	v_cvt_scalef32_pk_f32_fp4 v[50:51], v51, 1.0 op_sel:[1,1,0]
	v_pk_fma_f32 v[70:71], v[70:71], s[50:51], v[154:155] op_sel_hi:[1,0,1]
	v_pk_fma_f32 v[72:73], v[72:73], s[50:51], v[156:157] op_sel_hi:[1,0,1]
	v_pk_fma_f32 v[48:49], v[48:49], s[50:51], v[158:159] op_sel_hi:[1,0,1]
	v_pk_fma_f32 v[74:75], v[74:75], s[50:51], v[160:161] op_sel_hi:[1,0,1]
	v_pk_fma_f32 v[138:139], v[138:139], s[50:51], v[162:163] op_sel_hi:[1,0,1]
	v_pk_fma_f32 v[144:145], v[144:145], s[50:51], v[164:165] op_sel_hi:[1,0,1]
	v_pk_fma_f32 v[146:147], v[146:147], s[50:51], v[166:167] op_sel_hi:[1,0,1]
	v_pk_fma_f32 v[148:149], v[148:149], s[50:51], v[168:169] op_sel_hi:[1,0,1]
	v_pk_fma_f32 v[150:151], v[150:151], s[50:51], v[170:171] op_sel_hi:[1,0,1]
	v_pk_fma_f32 v[152:153], v[152:153], s[50:51], v[172:173] op_sel_hi:[1,0,1]
	v_pk_fma_f32 v[50:51], v[50:51], s[50:51], v[174:175] op_sel_hi:[1,0,1]
	v_readlane_b32 s50, v251, 1
	v_cvt_scalef32_pk_f32_fp4 v[154:155], v40, 1.0
	v_cvt_scalef32_pk_f32_fp4 v[156:157], v40, 1.0 op_sel:[1,0,0]
	v_cvt_scalef32_pk_f32_fp4 v[158:159], v40, 1.0 op_sel:[0,1,0]
	v_cvt_scalef32_pk_f32_fp4 v[160:161], v40, 1.0 op_sel:[1,1,0]
	v_pk_fma_f32 v[60:61], v[154:155], s[50:51], v[60:61] op_sel_hi:[1,0,1]
	v_pk_fma_f32 v[62:63], v[156:157], s[50:51], v[62:63] op_sel_hi:[1,0,1]
	v_pk_fma_f32 v[64:65], v[158:159], s[50:51], v[64:65] op_sel_hi:[1,0,1]
	v_cvt_scalef32_pk_f32_fp4 v[154:155], v41, 1.0
	v_cvt_scalef32_pk_f32_fp4 v[156:157], v41, 1.0 op_sel:[1,0,0]
	v_cvt_scalef32_pk_f32_fp4 v[158:159], v41, 1.0 op_sel:[0,1,0]
	v_cvt_scalef32_pk_f32_fp4 v[40:41], v41, 1.0 op_sel:[1,1,0]
	v_pk_fma_f32 v[68:69], v[154:155], s[50:51], v[68:69] op_sel_hi:[1,0,1]
	v_pk_fma_f32 v[70:71], v[156:157], s[50:51], v[70:71] op_sel_hi:[1,0,1]
	v_pk_fma_f32 v[72:73], v[158:159], s[50:51], v[72:73] op_sel_hi:[1,0,1]
	v_pk_fma_f32 v[40:41], v[40:41], s[50:51], v[48:49] op_sel_hi:[1,0,1]
	v_cvt_scalef32_pk_f32_fp4 v[48:49], v42, 1.0
	v_cvt_scalef32_pk_f32_fp4 v[154:155], v42, 1.0 op_sel:[1,0,0]
	v_cvt_scalef32_pk_f32_fp4 v[156:157], v42, 1.0 op_sel:[0,1,0]
	v_cvt_scalef32_pk_f32_fp4 v[158:159], v42, 1.0 op_sel:[1,1,0]
	v_pk_fma_f32 v[48:49], v[48:49], s[50:51], v[74:75] op_sel_hi:[1,0,1]
	v_pk_fma_f32 v[74:75], v[154:155], s[50:51], v[138:139] op_sel_hi:[1,0,1]
	v_pk_fma_f32 v[138:139], v[156:157], s[50:51], v[144:145] op_sel_hi:[1,0,1]
	v_pk_fma_f32 v[144:145], v[158:159], s[50:51], v[146:147] op_sel_hi:[1,0,1]
	v_cvt_scalef32_pk_f32_fp4 v[146:147], v43, 1.0
	v_cvt_scalef32_pk_f32_fp4 v[154:155], v43, 1.0 op_sel:[1,0,0]
	v_cvt_scalef32_pk_f32_fp4 v[156:157], v43, 1.0 op_sel:[0,1,0]
	v_cvt_scalef32_pk_f32_fp4 v[42:43], v43, 1.0 op_sel:[1,1,0]
	v_pk_fma_f32 v[66:67], v[160:161], s[50:51], v[66:67] op_sel_hi:[1,0,1]
	v_pk_fma_f32 v[146:147], v[146:147], s[50:51], v[148:149] op_sel_hi:[1,0,1]
	v_pk_fma_f32 v[148:149], v[154:155], s[50:51], v[150:151] op_sel_hi:[1,0,1]
	v_pk_fma_f32 v[150:151], v[156:157], s[50:51], v[152:153] op_sel_hi:[1,0,1]
	v_pk_fma_f32 v[42:43], v[42:43], s[50:51], v[50:51] op_sel_hi:[1,0,1]
	v_readlane_b32 s50, v251, 2
	v_cvt_scalef32_pk_f32_fp4 v[50:51], v32, 1.0
	v_cvt_scalef32_pk_f32_fp4 v[152:153], v32, 1.0 op_sel:[1,0,0]
	v_cvt_scalef32_pk_f32_fp4 v[154:155], v32, 1.0 op_sel:[0,1,0]
	v_cvt_scalef32_pk_f32_fp4 v[156:157], v32, 1.0 op_sel:[1,1,0]
	v_pk_fma_f32 v[50:51], v[50:51], s[50:51], v[60:61] op_sel_hi:[1,0,1]
	v_pk_fma_f32 v[60:61], v[152:153], s[50:51], v[62:63] op_sel_hi:[1,0,1]
	v_pk_fma_f32 v[62:63], v[154:155], s[50:51], v[64:65] op_sel_hi:[1,0,1]
	v_pk_fma_f32 v[64:65], v[156:157], s[50:51], v[66:67] op_sel_hi:[1,0,1]
	v_cvt_scalef32_pk_f32_fp4 v[66:67], v33, 1.0
	v_cvt_scalef32_pk_f32_fp4 v[152:153], v33, 1.0 op_sel:[1,0,0]
	v_cvt_scalef32_pk_f32_fp4 v[154:155], v33, 1.0 op_sel:[0,1,0]
	v_cvt_scalef32_pk_f32_fp4 v[32:33], v33, 1.0 op_sel:[1,1,0]
	v_pk_fma_f32 v[66:67], v[66:67], s[50:51], v[68:69] op_sel_hi:[1,0,1]
	v_pk_fma_f32 v[68:69], v[152:153], s[50:51], v[70:71] op_sel_hi:[1,0,1]
	v_pk_fma_f32 v[70:71], v[154:155], s[50:51], v[72:73] op_sel_hi:[1,0,1]
	v_pk_fma_f32 v[32:33], v[32:33], s[50:51], v[40:41] op_sel_hi:[1,0,1]
	v_cvt_scalef32_pk_f32_fp4 v[40:41], v34, 1.0
	v_cvt_scalef32_pk_f32_fp4 v[72:73], v34, 1.0 op_sel:[1,0,0]
	v_cvt_scalef32_pk_f32_fp4 v[152:153], v34, 1.0 op_sel:[0,1,0]
	v_cvt_scalef32_pk_f32_fp4 v[154:155], v34, 1.0 op_sel:[1,1,0]
	v_pk_fma_f32 v[40:41], v[40:41], s[50:51], v[48:49] op_sel_hi:[1,0,1]
	v_pk_fma_f32 v[48:49], v[72:73], s[50:51], v[74:75] op_sel_hi:[1,0,1]
	v_pk_fma_f32 v[72:73], v[152:153], s[50:51], v[138:139] op_sel_hi:[1,0,1]
	v_pk_fma_f32 v[74:75], v[154:155], s[50:51], v[144:145] op_sel_hi:[1,0,1]
	v_cvt_scalef32_pk_f32_fp4 v[138:139], v35, 1.0
	v_cvt_scalef32_pk_f32_fp4 v[144:145], v35, 1.0 op_sel:[1,0,0]
	v_cvt_scalef32_pk_f32_fp4 v[152:153], v35, 1.0 op_sel:[0,1,0]
	v_cvt_scalef32_pk_f32_fp4 v[34:35], v35, 1.0 op_sel:[1,1,0]
	v_pk_fma_f32 v[138:139], v[138:139], s[50:51], v[146:147] op_sel_hi:[1,0,1]
	v_pk_fma_f32 v[170:171], v[144:145], s[50:51], v[148:149] op_sel_hi:[1,0,1]
	v_pk_fma_f32 v[172:173], v[152:153], s[50:51], v[150:151] op_sel_hi:[1,0,1]
	v_pk_fma_f32 v[34:35], v[34:35], s[50:51], v[42:43] op_sel_hi:[1,0,1]
	v_readlane_b32 s50, v251, 3
	v_cvt_scalef32_pk_f32_fp4 v[42:43], v28, 1.0
	v_cvt_scalef32_pk_f32_fp4 v[146:147], v28, 1.0 op_sel:[1,0,0]
	v_cvt_scalef32_pk_f32_fp4 v[148:149], v28, 1.0 op_sel:[0,1,0]
	v_cvt_scalef32_pk_f32_fp4 v[150:151], v28, 1.0 op_sel:[1,1,0]
	v_pk_fma_f32 v[144:145], v[42:43], s[50:51], v[50:51] op_sel_hi:[1,0,1]
	v_pk_fma_f32 v[146:147], v[146:147], s[50:51], v[60:61] op_sel_hi:[1,0,1]
	v_cvt_scalef32_pk_f32_fp4 v[42:43], v29, 1.0
	v_cvt_scalef32_pk_f32_fp4 v[50:51], v29, 1.0 op_sel:[1,0,0]
	v_cvt_scalef32_pk_f32_fp4 v[60:61], v29, 1.0 op_sel:[0,1,0]
	v_cvt_scalef32_pk_f32_fp4 v[28:29], v29, 1.0 op_sel:[1,1,0]
	v_pk_fma_f32 v[158:159], v[28:29], s[50:51], v[32:33] op_sel_hi:[1,0,1]
	v_cvt_scalef32_pk_f32_fp4 v[28:29], v30, 1.0
	v_cvt_scalef32_pk_f32_fp4 v[32:33], v30, 1.0 op_sel:[1,0,0]
	v_pk_fma_f32 v[152:153], v[42:43], s[50:51], v[66:67] op_sel_hi:[1,0,1]
	v_pk_fma_f32 v[154:155], v[50:51], s[50:51], v[68:69] op_sel_hi:[1,0,1]
	v_cvt_scalef32_pk_f32_fp4 v[42:43], v30, 1.0 op_sel:[0,1,0]
	v_cvt_scalef32_pk_f32_fp4 v[50:51], v30, 1.0 op_sel:[1,1,0]
	v_pk_fma_f32 v[160:161], v[28:29], s[50:51], v[40:41] op_sel_hi:[1,0,1]
	v_pk_fma_f32 v[162:163], v[32:33], s[50:51], v[48:49] op_sel_hi:[1,0,1]
	v_cvt_scalef32_pk_f32_fp4 v[28:29], v31, 1.0
	v_cvt_scalef32_pk_f32_fp4 v[32:33], v31, 1.0 op_sel:[1,0,0]
	v_cvt_scalef32_pk_f32_fp4 v[40:41], v31, 1.0 op_sel:[0,1,0]
	v_cvt_scalef32_pk_f32_fp4 v[30:31], v31, 1.0 op_sel:[1,1,0]
	v_pk_fma_f32 v[148:149], v[148:149], s[50:51], v[62:63] op_sel_hi:[1,0,1]
	v_pk_fma_f32 v[150:151], v[150:151], s[50:51], v[64:65] op_sel_hi:[1,0,1]
	v_pk_fma_f32 v[156:157], v[60:61], s[50:51], v[70:71] op_sel_hi:[1,0,1]
	v_pk_fma_f32 v[164:165], v[42:43], s[50:51], v[72:73] op_sel_hi:[1,0,1]
	v_pk_fma_f32 v[166:167], v[50:51], s[50:51], v[74:75] op_sel_hi:[1,0,1]
	v_pk_fma_f32 v[168:169], v[28:29], s[50:51], v[138:139] op_sel_hi:[1,0,1]
	v_pk_fma_f32 v[170:171], v[32:33], s[50:51], v[170:171] op_sel_hi:[1,0,1]
	v_pk_fma_f32 v[172:173], v[40:41], s[50:51], v[172:173] op_sel_hi:[1,0,1]
	v_pk_fma_f32 v[174:175], v[30:31], s[50:51], v[34:35] op_sel_hi:[1,0,1]
	ds_read_b128 v[28:31], v250 offset:32
	ds_read_b32 v138, v249 offset:32
	v_mov_b32_e32 v250, 0
	v_mov_b32_e32 v251, 0
	s_waitcnt vmcnt(17)
	v_dot8c_i32_i4_e32 v250, v120, v24
	s_waitcnt lgkmcnt(1)
	v_readfirstlane_b32 s50, v28
	s_ashr_i32 s51, s50, 31
	s_lshl_b64 s[50:51], s[50:51], 10
	s_add_u32 s98, s100, s50
	s_addc_u32 s99, s101, s51
	global_load_dwordx4 v[72:75], v176, s[98:99]
	s_add_u32 s66, s86, s50
	s_addc_u32 s67, s87, s51
	v_readfirstlane_b32 s50, v29
	s_ashr_i32 s51, s50, 31
	s_lshl_b64 s[50:51], s[50:51], 10
	s_add_u32 s98, s100, s50
	s_addc_u32 s99, s101, s51
	global_load_dwordx4 v[48:51], v176, s[66:67]
	global_load_dwordx4 v[68:71], v176, s[98:99]
	s_add_u32 s66, s86, s50
	s_addc_u32 s67, s87, s51
	v_readfirstlane_b32 s50, v30
	s_waitcnt lgkmcnt(0)
	v_lshlrev_b32_e32 v138, 1, v138
	s_ashr_i32 s51, s50, 31
	v_ashrrev_i32_e32 v139, 31, v138
	s_lshl_b64 s[50:51], s[50:51], 10
	v_lshl_add_u64 v[138:139], v[138:139], 2, s[4:5]
	global_load_dwordx4 v[40:43], v176, s[66:67]
	v_dot8c_i32_i4_e32 v251, v120, v20
	global_load_dwordx2 v[138:139], v[138:139], off
	s_add_u32 s98, s100, s50
	s_addc_u32 s99, s101, s51
	global_load_dwordx4 v[64:67], v176, s[98:99]
	s_add_u32 s66, s86, s50
	s_addc_u32 s67, s87, s51
	v_readfirstlane_b32 s50, v31
	s_ashr_i32 s51, s50, 31
	s_lshl_b64 s[50:51], s[50:51], 10
	global_load_dwordx4 v[32:35], v176, s[66:67]
	s_add_u32 s98, s100, s50
	s_addc_u32 s99, s101, s51
	global_load_dwordx4 v[60:63], v176, s[98:99]
	s_add_u32 s66, s86, s50
	s_addc_u32 s67, s87, s51
	global_load_dwordx4 v[28:31], v176, s[66:67]
	v_dot8c_i32_i4_e32 v250, v121, v25
	v_dot8c_i32_i4_e32 v251, v121, v21
	v_dot8c_i32_i4_e32 v250, v122, v26
	v_dot8c_i32_i4_e32 v251, v122, v22
	v_mov_b32_e32 v121, 0
	v_mov_b32_e32 v122, 0
	s_waitcnt vmcnt(24)
	v_dot8c_i32_i4_e32 v121, v116, v24
	v_dot8c_i32_i4_e32 v122, v116, v20
	v_dot8c_i32_i4_e32 v121, v117, v25
	v_dot8c_i32_i4_e32 v122, v117, v21
	v_dot8c_i32_i4_e32 v121, v118, v26
	v_dot8c_i32_i4_e32 v122, v118, v22
	v_mov_b32_e32 v117, 0
	v_mov_b32_e32 v118, 0
	s_waitcnt vmcnt(22)
	v_dot8c_i32_i4_e32 v117, v112, v24
	v_dot8c_i32_i4_e32 v118, v112, v20
	v_dot8c_i32_i4_e32 v117, v113, v25
	v_dot8c_i32_i4_e32 v118, v113, v21
	v_dot8c_i32_i4_e32 v117, v114, v26
	v_dot8c_i32_i4_e32 v118, v114, v22
	v_mov_b32_e32 v113, 0
	v_mov_b32_e32 v114, 0
	s_waitcnt vmcnt(20)
	v_dot8c_i32_i4_e32 v113, v108, v24
	v_dot8c_i32_i4_e32 v114, v108, v20
	v_dot8c_i32_i4_e32 v113, v109, v25
	v_dot8c_i32_i4_e32 v114, v109, v21
	v_dot8c_i32_i4_e32 v250, v123, v27
	v_dot8c_i32_i4_e32 v251, v123, v23
	v_dot8c_i32_i4_e32 v121, v119, v27
	v_dot8c_i32_i4_e32 v122, v119, v23
	v_dot8c_i32_i4_e32 v113, v110, v26
	v_dot8c_i32_i4_e32 v114, v110, v22
	v_lshl_add_u32 v120, v250, 4, v251
	v_lshl_add_u32 v116, v121, 4, v122
	v_dot8c_i32_i4_e32 v117, v115, v27
	v_dot8c_i32_i4_e32 v118, v115, v23
	v_dot8c_i32_i4_e32 v113, v111, v27
	v_dot8c_i32_i4_e32 v114, v111, v23
	v_cvt_f32_i32_e32 v120, v120
	v_cvt_f32_i32_e32 v116, v116
	v_lshl_add_u32 v112, v117, 4, v118
	v_lshl_add_u32 v108, v113, 4, v114
	v_cvt_f32_i32_e32 v112, v112
	v_cvt_f32_i32_e32 v108, v108
	v_cndmask_b32_e64 v109, v116, v120, s[42:43]
	v_cndmask_b32_e64 v110, v120, v116, s[42:43]
	s_nop 1
	v_add_f32_dpp v109, v110, v109 quad_perm:[1,0,3,2] row_mask:0xf bank_mask:0xf bound_ctrl:1
	v_cndmask_b32_e64 v110, v108, v112, s[42:43]
	v_cndmask_b32_e64 v108, v112, v108, s[42:43]
	s_nop 1
	v_add_f32_dpp v108, v108, v110 quad_perm:[1,0,3,2] row_mask:0xf bank_mask:0xf bound_ctrl:1
	v_cndmask_b32_e64 v110, v108, v109, s[44:45]
	v_cndmask_b32_e64 v108, v109, v108, s[44:45]
	s_nop 1
	v_add_f32_dpp v108, v108, v110 quad_perm:[2,3,0,1] row_mask:0xf bank_mask:0xf bound_ctrl:1
	s_waitcnt vmcnt(18)
	v_mul_f32_e32 v110, v248, v142
	v_add_f32_dpp v108, v108, v108 row_ror:4 row_mask:0xf bank_mask:0xf bound_ctrl:1
	s_nop 1
	v_add_f32_dpp v108, v108, v108 row_ror:8 row_mask:0xf bank_mask:0xf bound_ctrl:1
	v_mov_b32_e32 v109, v108
	s_nop 1
	v_permlane32_swap_b32_e32 v108, v109
	v_add_f32_e32 v108, v108, v109
	v_mov_b32_e32 v109, v108
	s_nop 1
	v_permlane16_swap_b32_e32 v108, v109
	v_add_f32_e32 v108, v108, v109
	ds_read_b32 v109, v249 offset:512
	v_mul_f32_e32 v108, v110, v108
	v_fma_f32 v110, |v108|, s39, 1.0
	v_rcp_f32_e32 v110, v110
	v_cmp_gt_f32_e32 vcc, 0, v108
	v_fmamk_f32 v111, v110, 0x3f07dc22, v210
	v_fmaak_f32 v111, v110, v111, 0x3f35f0e3
	v_fmaak_f32 v111, v110, v111, 0xbe11a98e
	v_fmaak_f32 v111, v110, v111, 0x3e027906
	v_mul_f32_e32 v110, v110, v111
	v_mul_f32_e32 v111, v108, v108
	v_mul_f32_e32 v111, 0xbf38aa3b, v111
	v_exp_f32_e32 v111, v111
	s_nop 0
	v_mul_f32_e32 v110, v111, v110
	v_mul_f32_e32 v111, v108, v110
	v_fma_f32 v108, -v108, v110, v108
	v_cndmask_b32_e32 v108, v108, v111, vcc
	s_waitcnt lgkmcnt(0)
	v_mul_f32_e32 v108, v109, v108
	v_mul_f32_e32 v249, v143, v108
	s_nop 0
	v_readlane_b32 s50, v249, 0
	v_cvt_scalef32_pk_f32_fp4 v[108:109], v104, 1.0
	v_cvt_scalef32_pk_f32_fp4 v[110:111], v104, 1.0 op_sel:[1,0,0]
	v_cvt_scalef32_pk_f32_fp4 v[112:113], v104, 1.0 op_sel:[0,1,0]
	v_cvt_scalef32_pk_f32_fp4 v[114:115], v104, 1.0 op_sel:[1,1,0]
	v_cvt_scalef32_pk_f32_fp4 v[116:117], v105, 1.0
	v_pk_fma_f32 v[108:109], v[108:109], s[50:51], v[144:145] op_sel_hi:[1,0,1]
	v_pk_fma_f32 v[110:111], v[110:111], s[50:51], v[146:147] op_sel_hi:[1,0,1]
	v_pk_fma_f32 v[112:113], v[112:113], s[50:51], v[148:149] op_sel_hi:[1,0,1]
	v_pk_fma_f32 v[114:115], v[114:115], s[50:51], v[150:151] op_sel_hi:[1,0,1]
	v_pk_fma_f32 v[116:117], v[116:117], s[50:51], v[152:153] op_sel_hi:[1,0,1]
	v_cvt_scalef32_pk_f32_fp4 v[144:145], v106, 1.0 op_sel:[0,1,0]
	v_cvt_scalef32_pk_f32_fp4 v[146:147], v106, 1.0 op_sel:[1,1,0]
	v_cvt_scalef32_pk_f32_fp4 v[148:149], v107, 1.0
	v_cvt_scalef32_pk_f32_fp4 v[150:151], v107, 1.0 op_sel:[1,0,0]
	v_cvt_scalef32_pk_f32_fp4 v[152:153], v107, 1.0 op_sel:[0,1,0]
	v_cvt_scalef32_pk_f32_fp4 v[118:119], v105, 1.0 op_sel:[1,0,0]
	v_cvt_scalef32_pk_f32_fp4 v[120:121], v105, 1.0 op_sel:[0,1,0]
	v_cvt_scalef32_pk_f32_fp4 v[104:105], v105, 1.0 op_sel:[1,1,0]
	v_cvt_scalef32_pk_f32_fp4 v[122:123], v106, 1.0
	v_cvt_scalef32_pk_f32_fp4 v[142:143], v106, 1.0 op_sel:[1,0,0]
	v_pk_fma_f32 v[144:145], v[144:145], s[50:51], v[164:165] op_sel_hi:[1,0,1]
	v_pk_fma_f32 v[146:147], v[146:147], s[50:51], v[166:167] op_sel_hi:[1,0,1]
	v_cvt_scalef32_pk_f32_fp4 v[106:107], v107, 1.0 op_sel:[1,1,0]
	v_pk_fma_f32 v[148:149], v[148:149], s[50:51], v[168:169] op_sel_hi:[1,0,1]
	v_pk_fma_f32 v[150:151], v[150:151], s[50:51], v[170:171] op_sel_hi:[1,0,1]
	v_pk_fma_f32 v[152:153], v[152:153], s[50:51], v[172:173] op_sel_hi:[1,0,1]
	v_pk_fma_f32 v[118:119], v[118:119], s[50:51], v[154:155] op_sel_hi:[1,0,1]
	v_pk_fma_f32 v[120:121], v[120:121], s[50:51], v[156:157] op_sel_hi:[1,0,1]
	v_pk_fma_f32 v[104:105], v[104:105], s[50:51], v[158:159] op_sel_hi:[1,0,1]
	v_pk_fma_f32 v[122:123], v[122:123], s[50:51], v[160:161] op_sel_hi:[1,0,1]
	v_pk_fma_f32 v[142:143], v[142:143], s[50:51], v[162:163] op_sel_hi:[1,0,1]
	v_pk_fma_f32 v[106:107], v[106:107], s[50:51], v[174:175] op_sel_hi:[1,0,1]
	v_readlane_b32 s50, v249, 1
	v_cvt_scalef32_pk_f32_fp4 v[154:155], v100, 1.0
	v_cvt_scalef32_pk_f32_fp4 v[156:157], v100, 1.0 op_sel:[1,0,0]
	v_cvt_scalef32_pk_f32_fp4 v[158:159], v100, 1.0 op_sel:[0,1,0]
	v_cvt_scalef32_pk_f32_fp4 v[160:161], v100, 1.0 op_sel:[1,1,0]
	v_pk_fma_f32 v[108:109], v[154:155], s[50:51], v[108:109] op_sel_hi:[1,0,1]
	v_pk_fma_f32 v[110:111], v[156:157], s[50:51], v[110:111] op_sel_hi:[1,0,1]
	v_pk_fma_f32 v[112:113], v[158:159], s[50:51], v[112:113] op_sel_hi:[1,0,1]
	v_cvt_scalef32_pk_f32_fp4 v[154:155], v101, 1.0
	v_cvt_scalef32_pk_f32_fp4 v[156:157], v101, 1.0 op_sel:[1,0,0]
	v_cvt_scalef32_pk_f32_fp4 v[158:159], v101, 1.0 op_sel:[0,1,0]
	v_cvt_scalef32_pk_f32_fp4 v[100:101], v101, 1.0 op_sel:[1,1,0]
	v_pk_fma_f32 v[116:117], v[154:155], s[50:51], v[116:117] op_sel_hi:[1,0,1]
	v_pk_fma_f32 v[118:119], v[156:157], s[50:51], v[118:119] op_sel_hi:[1,0,1]
	v_pk_fma_f32 v[120:121], v[158:159], s[50:51], v[120:121] op_sel_hi:[1,0,1]
	v_pk_fma_f32 v[100:101], v[100:101], s[50:51], v[104:105] op_sel_hi:[1,0,1]
	v_cvt_scalef32_pk_f32_fp4 v[104:105], v102, 1.0
	v_cvt_scalef32_pk_f32_fp4 v[154:155], v102, 1.0 op_sel:[1,0,0]
	v_cvt_scalef32_pk_f32_fp4 v[156:157], v102, 1.0 op_sel:[0,1,0]
	v_cvt_scalef32_pk_f32_fp4 v[158:159], v102, 1.0 op_sel:[1,1,0]
	v_pk_fma_f32 v[104:105], v[104:105], s[50:51], v[122:123] op_sel_hi:[1,0,1]
	v_pk_fma_f32 v[122:123], v[154:155], s[50:51], v[142:143] op_sel_hi:[1,0,1]
	v_pk_fma_f32 v[142:143], v[156:157], s[50:51], v[144:145] op_sel_hi:[1,0,1]
	v_pk_fma_f32 v[144:145], v[158:159], s[50:51], v[146:147] op_sel_hi:[1,0,1]
	v_cvt_scalef32_pk_f32_fp4 v[146:147], v103, 1.0
	v_cvt_scalef32_pk_f32_fp4 v[154:155], v103, 1.0 op_sel:[1,0,0]
	v_cvt_scalef32_pk_f32_fp4 v[156:157], v103, 1.0 op_sel:[0,1,0]
	v_cvt_scalef32_pk_f32_fp4 v[102:103], v103, 1.0 op_sel:[1,1,0]
	v_pk_fma_f32 v[146:147], v[146:147], s[50:51], v[148:149] op_sel_hi:[1,0,1]
	v_pk_fma_f32 v[148:149], v[154:155], s[50:51], v[150:151] op_sel_hi:[1,0,1]
	v_pk_fma_f32 v[150:151], v[156:157], s[50:51], v[152:153] op_sel_hi:[1,0,1]
	v_pk_fma_f32 v[114:115], v[160:161], s[50:51], v[114:115] op_sel_hi:[1,0,1]
	v_pk_fma_f32 v[102:103], v[102:103], s[50:51], v[106:107] op_sel_hi:[1,0,1]
	v_readlane_b32 s50, v249, 2
	v_cvt_scalef32_pk_f32_fp4 v[106:107], v96, 1.0
	v_cvt_scalef32_pk_f32_fp4 v[152:153], v96, 1.0 op_sel:[1,0,0]
	v_cvt_scalef32_pk_f32_fp4 v[154:155], v96, 1.0 op_sel:[0,1,0]
	v_cvt_scalef32_pk_f32_fp4 v[156:157], v96, 1.0 op_sel:[1,1,0]
	v_pk_fma_f32 v[106:107], v[106:107], s[50:51], v[108:109] op_sel_hi:[1,0,1]
	v_pk_fma_f32 v[108:109], v[152:153], s[50:51], v[110:111] op_sel_hi:[1,0,1]
	v_pk_fma_f32 v[110:111], v[154:155], s[50:51], v[112:113] op_sel_hi:[1,0,1]
	v_pk_fma_f32 v[112:113], v[156:157], s[50:51], v[114:115] op_sel_hi:[1,0,1]
	v_cvt_scalef32_pk_f32_fp4 v[114:115], v97, 1.0
	v_cvt_scalef32_pk_f32_fp4 v[152:153], v97, 1.0 op_sel:[1,0,0]
	v_cvt_scalef32_pk_f32_fp4 v[154:155], v97, 1.0 op_sel:[0,1,0]
	v_cvt_scalef32_pk_f32_fp4 v[96:97], v97, 1.0 op_sel:[1,1,0]
	v_pk_fma_f32 v[114:115], v[114:115], s[50:51], v[116:117] op_sel_hi:[1,0,1]
	v_pk_fma_f32 v[116:117], v[152:153], s[50:51], v[118:119] op_sel_hi:[1,0,1]
	v_pk_fma_f32 v[118:119], v[154:155], s[50:51], v[120:121] op_sel_hi:[1,0,1]
	v_pk_fma_f32 v[96:97], v[96:97], s[50:51], v[100:101] op_sel_hi:[1,0,1]
	v_cvt_scalef32_pk_f32_fp4 v[100:101], v98, 1.0
	v_cvt_scalef32_pk_f32_fp4 v[120:121], v98, 1.0 op_sel:[1,0,0]
	v_cvt_scalef32_pk_f32_fp4 v[152:153], v98, 1.0 op_sel:[0,1,0]
	v_cvt_scalef32_pk_f32_fp4 v[154:155], v98, 1.0 op_sel:[1,1,0]
	v_pk_fma_f32 v[100:101], v[100:101], s[50:51], v[104:105] op_sel_hi:[1,0,1]
	v_pk_fma_f32 v[104:105], v[120:121], s[50:51], v[122:123] op_sel_hi:[1,0,1]
	v_pk_fma_f32 v[120:121], v[152:153], s[50:51], v[142:143] op_sel_hi:[1,0,1]
	v_pk_fma_f32 v[122:123], v[154:155], s[50:51], v[144:145] op_sel_hi:[1,0,1]
	v_cvt_scalef32_pk_f32_fp4 v[142:143], v99, 1.0
	v_cvt_scalef32_pk_f32_fp4 v[144:145], v99, 1.0 op_sel:[1,0,0]
	v_cvt_scalef32_pk_f32_fp4 v[152:153], v99, 1.0 op_sel:[0,1,0]
	v_cvt_scalef32_pk_f32_fp4 v[98:99], v99, 1.0 op_sel:[1,1,0]
	v_pk_fma_f32 v[142:143], v[142:143], s[50:51], v[146:147] op_sel_hi:[1,0,1]
	v_pk_fma_f32 v[144:145], v[144:145], s[50:51], v[148:149] op_sel_hi:[1,0,1]
	v_pk_fma_f32 v[146:147], v[152:153], s[50:51], v[150:151] op_sel_hi:[1,0,1]
	v_pk_fma_f32 v[98:99], v[98:99], s[50:51], v[102:103] op_sel_hi:[1,0,1]
	v_readlane_b32 s50, v249, 3
	v_cvt_scalef32_pk_f32_fp4 v[102:103], v92, 1.0
	v_cvt_scalef32_pk_f32_fp4 v[148:149], v92, 1.0 op_sel:[1,0,0]
	v_cvt_scalef32_pk_f32_fp4 v[150:151], v92, 1.0 op_sel:[0,1,0]
	v_cvt_scalef32_pk_f32_fp4 v[154:155], v92, 1.0 op_sel:[1,1,0]
	v_pk_fma_f32 v[152:153], v[102:103], s[50:51], v[106:107] op_sel_hi:[1,0,1]
	v_pk_fma_f32 v[174:175], v[148:149], s[50:51], v[108:109] op_sel_hi:[1,0,1]
	v_cvt_scalef32_pk_f32_fp4 v[102:103], v93, 1.0
	v_cvt_scalef32_pk_f32_fp4 v[106:107], v93, 1.0 op_sel:[1,0,0]
	v_cvt_scalef32_pk_f32_fp4 v[108:109], v93, 1.0 op_sel:[0,1,0]
	v_cvt_scalef32_pk_f32_fp4 v[92:93], v93, 1.0 op_sel:[1,1,0]
	v_pk_fma_f32 v[162:163], v[92:93], s[50:51], v[96:97] op_sel_hi:[1,0,1]
	v_cvt_scalef32_pk_f32_fp4 v[92:93], v94, 1.0
	v_cvt_scalef32_pk_f32_fp4 v[96:97], v94, 1.0 op_sel:[1,0,0]
	v_pk_fma_f32 v[168:169], v[102:103], s[50:51], v[114:115] op_sel_hi:[1,0,1]
	v_pk_fma_f32 v[166:167], v[106:107], s[50:51], v[116:117] op_sel_hi:[1,0,1]
	v_cvt_scalef32_pk_f32_fp4 v[102:103], v94, 1.0 op_sel:[0,1,0]
	v_cvt_scalef32_pk_f32_fp4 v[106:107], v94, 1.0 op_sel:[1,1,0]
	v_pk_fma_f32 v[160:161], v[92:93], s[50:51], v[100:101] op_sel_hi:[1,0,1]
	v_pk_fma_f32 v[158:159], v[96:97], s[50:51], v[104:105] op_sel_hi:[1,0,1]
	v_cvt_scalef32_pk_f32_fp4 v[92:93], v95, 1.0
	v_cvt_scalef32_pk_f32_fp4 v[96:97], v95, 1.0 op_sel:[1,0,0]
	v_cvt_scalef32_pk_f32_fp4 v[100:101], v95, 1.0 op_sel:[0,1,0]
	v_cvt_scalef32_pk_f32_fp4 v[94:95], v95, 1.0 op_sel:[1,1,0]
	v_pk_fma_f32 v[172:173], v[150:151], s[50:51], v[110:111] op_sel_hi:[1,0,1]
	v_pk_fma_f32 v[170:171], v[154:155], s[50:51], v[112:113] op_sel_hi:[1,0,1]
	v_pk_fma_f32 v[164:165], v[108:109], s[50:51], v[118:119] op_sel_hi:[1,0,1]
	v_pk_fma_f32 v[156:157], v[102:103], s[50:51], v[120:121] op_sel_hi:[1,0,1]
	v_pk_fma_f32 v[154:155], v[106:107], s[50:51], v[122:123] op_sel_hi:[1,0,1]
	v_pk_fma_f32 v[150:151], v[92:93], s[50:51], v[142:143] op_sel_hi:[1,0,1]
	v_pk_fma_f32 v[148:149], v[96:97], s[50:51], v[144:145] op_sel_hi:[1,0,1]
	v_pk_fma_f32 v[146:147], v[100:101], s[50:51], v[146:147] op_sel_hi:[1,0,1]
	v_pk_fma_f32 v[144:145], v[94:95], s[50:51], v[98:99] op_sel_hi:[1,0,1]
	s_add_i32 s8, s8, 48
	s_add_i32 s6, s6, 12
	s_cmpk_gt_u32 s6, 0x6b
	s_cbranch_scc0 .LBB0_776
	v_mov_b32_e32 v92, v3
	v_mov_b32_e32 v93, v3
	s_waitcnt vmcnt(17)
	v_dot8c_i32_i4_e32 v92, v88, v24
	v_dot8c_i32_i4_e32 v93, v88, v20
	v_dot8c_i32_i4_e32 v92, v89, v25
	v_dot8c_i32_i4_e32 v93, v89, v21
	v_dot8c_i32_i4_e32 v92, v90, v26
	v_dot8c_i32_i4_e32 v93, v90, v22
	v_mov_b32_e32 v89, v3
	v_mov_b32_e32 v90, v3
	s_waitcnt vmcnt(15)
	v_dot8c_i32_i4_e32 v89, v84, v24
	v_dot8c_i32_i4_e32 v90, v84, v20
	v_dot8c_i32_i4_e32 v89, v85, v25
	v_dot8c_i32_i4_e32 v90, v85, v21
	v_dot8c_i32_i4_e32 v89, v86, v26
	v_dot8c_i32_i4_e32 v90, v86, v22
	v_mov_b32_e32 v85, v3
	v_mov_b32_e32 v86, v3
	s_waitcnt vmcnt(12)
	v_dot8c_i32_i4_e32 v85, v80, v24
	v_dot8c_i32_i4_e32 v86, v80, v20
	v_dot8c_i32_i4_e32 v85, v81, v25
	v_dot8c_i32_i4_e32 v86, v81, v21
	v_dot8c_i32_i4_e32 v85, v82, v26
	v_dot8c_i32_i4_e32 v86, v82, v22
	v_mov_b32_e32 v81, v3
	v_mov_b32_e32 v82, v3
	s_waitcnt vmcnt(10)
	v_dot8c_i32_i4_e32 v81, v76, v24
	v_dot8c_i32_i4_e32 v82, v76, v20
	v_dot8c_i32_i4_e32 v81, v77, v25
	v_dot8c_i32_i4_e32 v82, v77, v21
	v_dot8c_i32_i4_e32 v92, v91, v27
	v_dot8c_i32_i4_e32 v93, v91, v23
	v_dot8c_i32_i4_e32 v89, v87, v27
	v_dot8c_i32_i4_e32 v90, v87, v23
	v_dot8c_i32_i4_e32 v81, v78, v26
	v_dot8c_i32_i4_e32 v82, v78, v22
	v_lshl_add_u32 v88, v92, 4, v93
	v_lshl_add_u32 v84, v89, 4, v90
	v_dot8c_i32_i4_e32 v85, v83, v27
	v_dot8c_i32_i4_e32 v86, v83, v23
	v_dot8c_i32_i4_e32 v81, v79, v27
	v_dot8c_i32_i4_e32 v82, v79, v23
	v_cvt_f32_i32_e32 v88, v88
	v_cvt_f32_i32_e32 v84, v84
	v_lshl_add_u32 v80, v85, 4, v86
	v_lshl_add_u32 v76, v81, 4, v82
	v_cvt_f32_i32_e32 v80, v80
	v_cvt_f32_i32_e32 v76, v76
	v_cndmask_b32_e64 v77, v84, v88, s[42:43]
	v_cndmask_b32_e64 v78, v88, v84, s[42:43]
	s_nop 1
	v_add_f32_dpp v77, v78, v77 quad_perm:[1,0,3,2] row_mask:0xf bank_mask:0xf bound_ctrl:1
	v_cndmask_b32_e64 v78, v76, v80, s[42:43]
	v_cndmask_b32_e64 v76, v80, v76, s[42:43]
	s_nop 1
	v_add_f32_dpp v76, v76, v78 quad_perm:[1,0,3,2] row_mask:0xf bank_mask:0xf bound_ctrl:1
	v_cndmask_b32_e64 v78, v76, v77, s[44:45]
	v_cndmask_b32_e64 v76, v77, v76, s[44:45]
	s_nop 1
	v_add_f32_dpp v76, v76, v78 quad_perm:[2,3,0,1] row_mask:0xf bank_mask:0xf bound_ctrl:1
	s_nop 1
	v_add_f32_dpp v76, v76, v76 row_ror:4 row_mask:0xf bank_mask:0xf bound_ctrl:1
	s_nop 1
	v_add_f32_dpp v76, v76, v76 row_ror:8 row_mask:0xf bank_mask:0xf bound_ctrl:1
	v_mov_b32_e32 v77, v76
	s_nop 1
	v_permlane32_swap_b32_e32 v76, v77
	v_add_f32_e32 v76, v76, v77
	v_mov_b32_e32 v77, v76
	s_nop 1
	v_permlane16_swap_b32_e32 v76, v77
	v_add_f32_e32 v76, v76, v77
	v_mul_f32_e32 v77, v248, v140
	v_mul_f32_e32 v76, v77, v76
	v_fma_f32 v77, |v76|, s39, 1.0
	v_rcp_f32_e32 v77, v77
	v_mul_f32_e32 v80, v76, v76
	v_mul_f32_e32 v80, 0xbf38aa3b, v80
	v_exp_f32_e32 v80, v80
	v_fmamk_f32 v79, v77, 0x3f07dc22, v210
	v_fmaak_f32 v79, v77, v79, 0x3f35f0e3
	v_fmaak_f32 v79, v77, v79, 0xbe11a98e
	ds_read_b32 v78, v184 offset:4320
	v_fmaak_f32 v79, v77, v79, 0x3e027906
	v_mul_f32_e32 v77, v77, v79
	v_mul_f32_e32 v77, v80, v77
	v_mul_f32_e32 v79, v76, v77
	v_fma_f32 v77, -v76, v77, v76
	v_cmp_gt_f32_e32 vcc, 0, v76
	s_nop 1
	v_cndmask_b32_e32 v76, v77, v79, vcc
	s_waitcnt lgkmcnt(0)
	v_mul_f32_e32 v76, v78, v76
	v_mul_f32_e32 v76, v141, v76
	s_nop 0
	v_readlane_b32 s8, v76, 0
	v_readlane_b32 s62, v76, 1
	v_readlane_b32 s58, v76, 2
	v_readlane_b32 s56, v76, 3
	v_mov_b32_e32 v76, v3
	v_mov_b32_e32 v77, v3
	s_waitcnt vmcnt(8)
	v_dot8c_i32_i4_e32 v76, v72, v24
	v_dot8c_i32_i4_e32 v77, v72, v20
	v_dot8c_i32_i4_e32 v76, v73, v25
	v_dot8c_i32_i4_e32 v77, v73, v21
	v_dot8c_i32_i4_e32 v76, v74, v26
	v_dot8c_i32_i4_e32 v77, v74, v22
	v_mov_b32_e32 v73, v3
	v_mov_b32_e32 v74, v3
	s_waitcnt vmcnt(6)
	v_dot8c_i32_i4_e32 v73, v68, v24
	v_dot8c_i32_i4_e32 v74, v68, v20
	v_dot8c_i32_i4_e32 v73, v69, v25
	v_dot8c_i32_i4_e32 v74, v69, v21
	v_dot8c_i32_i4_e32 v73, v70, v26
	v_dot8c_i32_i4_e32 v74, v70, v22
	v_mov_b32_e32 v69, v3
	v_mov_b32_e32 v70, v3
	s_waitcnt vmcnt(3)
	v_dot8c_i32_i4_e32 v69, v64, v24
	v_dot8c_i32_i4_e32 v70, v64, v20
	v_dot8c_i32_i4_e32 v69, v65, v25
	v_dot8c_i32_i4_e32 v70, v65, v21
	v_mov_b32_e32 v65, v3
	s_waitcnt vmcnt(1)
	v_dot8c_i32_i4_e32 v65, v60, v24
	v_mov_b32_e32 v24, v3
	v_dot8c_i32_i4_e32 v24, v60, v20
	v_dot8c_i32_i4_e32 v65, v61, v25
	v_dot8c_i32_i4_e32 v24, v61, v21
	v_dot8c_i32_i4_e32 v76, v75, v27
	v_dot8c_i32_i4_e32 v77, v75, v23
	v_dot8c_i32_i4_e32 v73, v71, v27
	v_dot8c_i32_i4_e32 v74, v71, v23
	v_dot8c_i32_i4_e32 v69, v66, v26
	v_dot8c_i32_i4_e32 v70, v66, v22
	v_dot8c_i32_i4_e32 v65, v62, v26
	v_dot8c_i32_i4_e32 v24, v62, v22
	v_lshl_add_u32 v72, v76, 4, v77
	v_lshl_add_u32 v68, v73, 4, v74
	v_dot8c_i32_i4_e32 v69, v67, v27
	v_dot8c_i32_i4_e32 v70, v67, v23
	v_dot8c_i32_i4_e32 v65, v63, v27
	v_dot8c_i32_i4_e32 v24, v63, v23
	v_cvt_f32_i32_e32 v72, v72
	v_cvt_f32_i32_e32 v68, v68
	v_lshl_add_u32 v64, v69, 4, v70
	v_lshl_add_u32 v20, v65, 4, v24
	v_cvt_f32_i32_e32 v64, v64
	v_cvt_f32_i32_e32 v20, v20
	v_cndmask_b32_e64 v21, v68, v72, s[42:43]
	v_cndmask_b32_e64 v22, v72, v68, s[42:43]
	s_nop 1
	v_add_f32_dpp v21, v22, v21 quad_perm:[1,0,3,2] row_mask:0xf bank_mask:0xf bound_ctrl:1
	v_cndmask_b32_e64 v22, v20, v64, s[42:43]
	v_cndmask_b32_e64 v20, v64, v20, s[42:43]
	s_nop 1
	v_add_f32_dpp v20, v20, v22 quad_perm:[1,0,3,2] row_mask:0xf bank_mask:0xf bound_ctrl:1
	v_cndmask_b32_e64 v22, v20, v21, s[44:45]
	v_cndmask_b32_e64 v20, v21, v20, s[44:45]
	s_nop 1
	v_add_f32_dpp v20, v20, v22 quad_perm:[2,3,0,1] row_mask:0xf bank_mask:0xf bound_ctrl:1
	s_nop 1
	v_add_f32_dpp v20, v20, v20 row_ror:4 row_mask:0xf bank_mask:0xf bound_ctrl:1
	s_nop 1
	v_add_f32_dpp v20, v20, v20 row_ror:8 row_mask:0xf bank_mask:0xf bound_ctrl:1
	v_mov_b32_e32 v21, v20
	s_nop 1
	v_permlane32_swap_b32_e32 v20, v21
	v_add_f32_e32 v20, v20, v21
	v_mov_b32_e32 v21, v20
	s_nop 1
	v_permlane16_swap_b32_e32 v20, v21
	v_add_f32_e32 v20, v20, v21
	v_mul_f32_e32 v21, v248, v138
	v_mul_f32_e32 v20, v21, v20
	v_fma_f32 v21, |v20|, s39, 1.0
	v_rcp_f32_e32 v21, v21
	v_mul_f32_e32 v24, v20, v20
	v_mul_f32_e32 v24, 0xbf38aa3b, v24
	v_exp_f32_e32 v24, v24
	v_fmamk_f32 v23, v21, 0x3f07dc22, v210
	v_fmaak_f32 v23, v21, v23, 0x3f35f0e3
	v_fmaak_f32 v23, v21, v23, 0xbe11a98e
	ds_read_b32 v22, v184 offset:4336
	v_fmaak_f32 v23, v21, v23, 0x3e027906
	v_mul_f32_e32 v21, v21, v23
	v_mul_f32_e32 v21, v24, v21
	v_mul_f32_e32 v23, v20, v21
	v_fma_f32 v21, -v20, v21, v20
	v_cmp_gt_f32_e32 vcc, 0, v20
	s_nop 1
	v_cndmask_b32_e32 v20, v21, v23, vcc
	s_waitcnt lgkmcnt(0)
	v_mul_f32_e32 v20, v22, v20
	v_mul_f32_e32 v20, v139, v20
	s_nop 0
	v_readlane_b32 s64, v20, 0
	v_readlane_b32 s60, v20, 1
	v_readlane_b32 s50, v20, 2
	v_readlane_b32 s6, v20, 3
	v_readfirstlane_b32 s52, v247
	s_cmp_ge_i32 s52, s26
	s_cselect_b64 s[54:55], -1, 0
	s_cmp_lt_i32 s52, s26
	s_cbranch_scc0 .LBB0_779
	s_ashr_i32 s53, s52, 31
	s_lshl_b64 s[80:81], s[52:53], 12
	v_lshl_add_u64 v[4:5], v[132:133], 0, s[80:81]
	global_load_dwordx4 v[8:11], v[4:5], off offset:48
	global_load_dwordx4 v[12:15], v[4:5], off offset:32
	global_load_dwordx4 v[16:19], v[4:5], off offset:16
	s_nop 0
	global_load_dwordx4 v[4:7], v[4:5], off
